# v5: adds unscaled fp8 MFMA form (unit scales dropped, same e4m3 math) and NSA q-row loads issued together instead of 8 serial round trips
# speedup vs baseline: 1.0232x; 1.0091x over previous
.LBB0_214:
	s_ashr_i32 s21, s20, 31
	s_lshl_b64 s[22:23], s[20:21], 19
	s_add_u32 s22, s34, s22
	s_addc_u32 s23, s35, s23
	s_and_b64 s[24:25], s[8:9], exec
	ds_read_b128 v[2:5], v175
	ds_read_b128 v[6:9], v175 offset:1024
	ds_read_b128 v[10:13], v175 offset:2048
	ds_read_b128 v[14:17], v175 offset:3072
	s_cselect_b32 s13, s23, s31
	s_cselect_b32 s21, s22, s30
	s_ashr_i32 s15, s14, 31
	s_lshl_b64 s[24:25], s[14:15], 19
	s_add_u32 s24, s36, s24
	s_addc_u32 s25, s37, s25
	s_and_b64 s[8:9], s[8:9], exec
	s_cselect_b32 s15, s25, s29
	s_cselect_b32 s51, s24, s28
	s_add_u32 s8, s30, 0x40080
	s_addc_u32 s9, s31, 0
	s_add_i32 s52, s27, 0xc000
	v_lshl_add_u64 v[54:55], s[8:9], 0, v[156:157]
	s_mov_b32 m0, s52
	s_add_i32 s53, s27, 0xe000
	ds_read_b128 v[22:25], v176
	ds_read_b128 v[26:29], v176 offset:1024
	ds_read_b128 v[30:33], v176 offset:2048
	ds_read_b128 v[34:37], v176 offset:3072
	ds_read_b128 v[38:41], v176 offset:4096
	ds_read_b128 v[42:45], v176 offset:5120
	ds_read_b128 v[46:49], v176 offset:6144
	ds_read_b128 v[50:53], v176 offset:7168
	global_load_lds_dwordx4 v[54:55], off
	v_lshl_add_u64 v[54:55], s[8:9], 0, v[152:153]
	s_mov_b32 m0, s53
	s_nop 0
	global_load_lds_dwordx4 v[54:55], off
	s_waitcnt lgkmcnt(8)
	s_barrier
	s_waitcnt lgkmcnt(0)
	s_setprio 1
	s_waitcnt lgkmcnt(0)
	v_mfma_f32_16x16x128_f8f6f4 v[138:141], v[2:9], v[22:29], 0
	v_mfma_f32_16x16x128_f8f6f4 v[134:137], v[10:17], v[22:29], 0
	v_mfma_f32_16x16x128_f8f6f4 v[122:125], v[2:9], v[30:37], 0
	v_mfma_f32_16x16x128_f8f6f4 v[118:121], v[10:17], v[30:37], 0
	v_mfma_f32_16x16x128_f8f6f4 v[98:101], v[2:9], v[38:45], 0
	v_mfma_f32_16x16x128_f8f6f4 v[90:93], v[10:17], v[38:45], 0
	v_mfma_f32_16x16x128_f8f6f4 v[70:73], v[2:9], v[46:53], 0
	v_mfma_f32_16x16x128_f8f6f4 v[58:61], v[10:17], v[46:53], 0
	s_setprio 0
	s_barrier
	v_lshl_add_u64 v[170:171], s[28:29], 0, v[154:155]
	s_add_i32 s54, s47, s38
	v_lshl_add_u64 v[54:55], v[170:171], 0, s[10:11]
	s_mov_b32 m0, s54
	v_lshl_add_u64 v[172:173], s[28:29], 0, v[150:151]
	s_add_i32 s55, s54, 0x2000
	ds_read_b128 v[178:181], v177
	ds_read_b128 v[182:185], v177 offset:1024
	ds_read_b128 v[186:189], v177 offset:2048
	ds_read_b128 v[190:193], v177 offset:3072
	global_load_lds_dwordx4 v[54:55], off
	v_lshl_add_u64 v[54:55], v[172:173], 0, s[10:11]
	s_mov_b32 m0, s55
	s_nop 0
	global_load_lds_dwordx4 v[54:55], off
	s_barrier
	s_waitcnt lgkmcnt(0)
	s_setprio 1
	s_waitcnt lgkmcnt(0)
	v_mfma_f32_16x16x128_f8f6f4 v[146:149], v[178:185], v[22:29], 0
	v_mfma_f32_16x16x128_f8f6f4 v[142:145], v[186:193], v[22:29], 0
	v_mfma_f32_16x16x128_f8f6f4 v[130:133], v[178:185], v[30:37], 0
	v_mfma_f32_16x16x128_f8f6f4 v[126:129], v[186:193], v[30:37], 0
	v_mfma_f32_16x16x128_f8f6f4 v[114:117], v[178:185], v[38:45], 0
	v_mfma_f32_16x16x128_f8f6f4 v[110:113], v[186:193], v[38:45], 0
	v_mfma_f32_16x16x128_f8f6f4 v[82:85], v[178:185], v[46:53], 0
	v_mfma_f32_16x16x128_f8f6f4 v[78:81], v[186:193], v[46:53], 0
	s_setprio 0
	v_lshl_add_u64 v[166:167], s[30:31], 0, v[156:157]
	s_mov_b32 m0, s27
	v_lshl_add_u64 v[22:23], v[166:167], 0, s[10:11]
	v_lshl_add_u64 v[168:169], s[30:31], 0, v[152:153]
	s_barrier
	ds_read_b128 v[194:197], v176 offset:16384
	ds_read_b128 v[198:201], v176 offset:17408
	ds_read_b128 v[202:205], v176 offset:18432
	ds_read_b128 v[206:209], v176 offset:19456
	ds_read_b128 v[210:213], v176 offset:20480
	ds_read_b128 v[214:217], v176 offset:21504
	ds_read_b128 v[218:221], v176 offset:22528
	ds_read_b128 v[222:225], v176 offset:23552
	global_load_lds_dwordx4 v[22:23], off
	v_lshl_add_u64 v[22:23], v[168:169], 0, s[10:11]
	s_mov_b32 m0, s41
	s_nop 0
	global_load_lds_dwordx4 v[22:23], off
	s_barrier
	s_waitcnt lgkmcnt(0)
	s_setprio 1
	s_waitcnt lgkmcnt(0)
	v_mfma_f32_16x16x128_f8f6f4 v[94:97], v[2:9], v[194:201], 0
	v_mfma_f32_16x16x128_f8f6f4 v[86:89], v[10:17], v[194:201], 0
	v_mfma_f32_16x16x128_f8f6f4 v[66:69], v[2:9], v[202:209], 0
	v_mfma_f32_16x16x128_f8f6f4 v[54:57], v[10:17], v[202:209], 0
	v_mfma_f32_16x16x128_f8f6f4 v[46:49], v[2:9], v[210:217], 0
	v_mfma_f32_16x16x128_f8f6f4 v[38:41], v[10:17], v[210:217], 0
	v_mfma_f32_16x16x128_f8f6f4 v[30:33], v[2:9], v[218:225], 0
	v_mfma_f32_16x16x128_f8f6f4 v[22:25], v[10:17], v[218:225], 0
	s_setprio 0
	s_barrier
	s_add_u32 s8, s28, 0x40100
	s_addc_u32 s9, s29, 0
	s_add_i32 s56, s48, s38
	v_lshl_add_u64 v[2:3], s[8:9], 0, v[154:155]
	s_mov_b32 m0, s56
	s_add_i32 s57, s56, 0x2000
	global_load_lds_dwordx4 v[2:3], off
	v_lshl_add_u64 v[2:3], s[8:9], 0, v[150:151]
	s_mov_b32 m0, s57
	s_nop 0
	global_load_lds_dwordx4 v[2:3], off
	s_waitcnt vmcnt(6)
	s_barrier
	s_setprio 1
	v_mfma_f32_16x16x128_f8f6f4 v[106:109], v[178:185], v[194:201], 0
	v_mfma_f32_16x16x128_f8f6f4 v[102:105], v[186:193], v[194:201], 0
	v_mfma_f32_16x16x128_f8f6f4 v[74:77], v[178:185], v[202:209], 0
	v_mfma_f32_16x16x128_f8f6f4 v[62:65], v[186:193], v[202:209], 0
	v_mfma_f32_16x16x128_f8f6f4 v[50:53], v[178:185], v[210:217], 0
	v_mfma_f32_16x16x128_f8f6f4 v[42:45], v[186:193], v[210:217], 0
	v_mfma_f32_16x16x128_f8f6f4 v[34:37], v[178:185], v[218:225], 0
	v_mfma_f32_16x16x128_f8f6f4 v[26:29], v[186:193], v[218:225], 0
	s_setprio 0
	s_add_i32 s58, 0, 0x18000
	v_add_u32_e32 v178, s58, v174
	s_barrier
	ds_read_b128 v[2:5], v178
	ds_read_b128 v[6:9], v178 offset:1024
	ds_read_b128 v[10:13], v178 offset:2048
	ds_read_b128 v[14:17], v178 offset:3072
	s_add_u32 s8, s30, 0x40100
	s_addc_u32 s9, s31, 0
	s_mov_b32 m0, s42
	v_lshl_add_u64 v[212:213], s[8:9], 0, v[156:157]
	ds_read_b128 v[180:183], v176 offset:32768
	ds_read_b128 v[184:187], v176 offset:33792
	ds_read_b128 v[188:191], v176 offset:34816
	ds_read_b128 v[192:195], v176 offset:35840
	ds_read_b128 v[196:199], v176 offset:36864
	ds_read_b128 v[200:203], v176 offset:37888
	ds_read_b128 v[204:207], v176 offset:38912
	ds_read_b128 v[208:211], v176 offset:39936
	global_load_lds_dwordx4 v[212:213], off
	v_lshl_add_u64 v[212:213], s[8:9], 0, v[152:153]
	s_mov_b32 m0, s43
	s_nop 0
	global_load_lds_dwordx4 v[212:213], off
	s_waitcnt lgkmcnt(8)
	s_barrier
	s_waitcnt lgkmcnt(0)
	s_setprio 1
	s_waitcnt lgkmcnt(0)
	v_mfma_f32_16x16x128_f8f6f4 v[138:141], v[2:9], v[180:187], v[138:141]
	v_mfma_f32_16x16x128_f8f6f4 v[134:137], v[10:17], v[180:187], v[134:137]
	v_mfma_f32_16x16x128_f8f6f4 v[122:125], v[2:9], v[188:195], v[122:125]
	v_mfma_f32_16x16x128_f8f6f4 v[118:121], v[10:17], v[188:195], v[118:121]
	v_mfma_f32_16x16x128_f8f6f4 v[98:101], v[2:9], v[196:203], v[98:101]
	v_mfma_f32_16x16x128_f8f6f4 v[90:93], v[10:17], v[196:203], v[90:93]
	v_mfma_f32_16x16x128_f8f6f4 v[70:73], v[2:9], v[204:211], v[70:73]
	v_mfma_f32_16x16x128_f8f6f4 v[58:61], v[10:17], v[204:211], v[58:61]
	s_setprio 0
	s_barrier
	s_add_i32 s60, 0, 0x1c000
	s_add_i32 s58, s58, s38
	v_add_u32_e32 v179, s60, v174
	v_lshl_add_u64 v[170:171], v[170:171], 0, s[16:17]
	s_mov_b32 m0, s58
	s_add_i32 s59, s58, 0x2000
	ds_read_b128 v[212:215], v179
	ds_read_b128 v[216:219], v179 offset:1024
	ds_read_b128 v[220:223], v179 offset:2048
	ds_read_b128 v[224:227], v179 offset:3072
	global_load_lds_dwordx4 v[170:171], off
	v_lshl_add_u64 v[170:171], v[172:173], 0, s[16:17]
	s_mov_b32 m0, s59
	s_nop 0
	global_load_lds_dwordx4 v[170:171], off
	s_barrier
	s_waitcnt lgkmcnt(0)
	s_setprio 1
	s_waitcnt lgkmcnt(0)
	v_mfma_f32_16x16x128_f8f6f4 v[146:149], v[212:219], v[180:187], v[146:149]
	v_mfma_f32_16x16x128_f8f6f4 v[142:145], v[220:227], v[180:187], v[142:145]
	v_mfma_f32_16x16x128_f8f6f4 v[130:133], v[212:219], v[188:195], v[130:133]
	v_mfma_f32_16x16x128_f8f6f4 v[126:129], v[220:227], v[188:195], v[126:129]
	v_mfma_f32_16x16x128_f8f6f4 v[114:117], v[212:219], v[196:203], v[114:117]
	v_mfma_f32_16x16x128_f8f6f4 v[110:113], v[220:227], v[196:203], v[110:113]
	v_mfma_f32_16x16x128_f8f6f4 v[82:85], v[212:219], v[204:211], v[82:85]
	v_mfma_f32_16x16x128_f8f6f4 v[78:81], v[220:227], v[204:211], v[78:81]
	s_setprio 0
	s_mov_b32 m0, s44
	v_lshl_add_u64 v[166:167], v[166:167], 0, s[16:17]
	s_barrier
	ds_read_b128 v[180:183], v176 offset:49152
	ds_read_b128 v[184:187], v176 offset:50176
	ds_read_b128 v[188:191], v176 offset:51200
	ds_read_b128 v[192:195], v176 offset:52224
	ds_read_b128 v[196:199], v176 offset:53248
	ds_read_b128 v[200:203], v176 offset:54272
	ds_read_b128 v[204:207], v176 offset:55296
	ds_read_b128 v[208:211], v176 offset:56320
	global_load_lds_dwordx4 v[166:167], off
	v_lshl_add_u64 v[166:167], v[168:169], 0, s[16:17]
	s_mov_b32 m0, s45
	s_nop 0
	global_load_lds_dwordx4 v[166:167], off
	s_barrier
	s_waitcnt lgkmcnt(0)
	s_setprio 1
	s_waitcnt lgkmcnt(0)
	v_mfma_f32_16x16x128_f8f6f4 v[94:97], v[2:9], v[180:187], v[94:97]
	v_mfma_f32_16x16x128_f8f6f4 v[86:89], v[10:17], v[180:187], v[86:89]
	v_mfma_f32_16x16x128_f8f6f4 v[66:69], v[2:9], v[188:195], v[66:69]
	v_mfma_f32_16x16x128_f8f6f4 v[54:57], v[10:17], v[188:195], v[54:57]
	v_mfma_f32_16x16x128_f8f6f4 v[46:49], v[2:9], v[196:203], v[46:49]
	v_mfma_f32_16x16x128_f8f6f4 v[38:41], v[10:17], v[196:203], v[38:41]
	v_mfma_f32_16x16x128_f8f6f4 v[30:33], v[2:9], v[204:211], v[30:33]
	v_mfma_f32_16x16x128_f8f6f4 v[22:25], v[10:17], v[204:211], v[22:25]
	s_setprio 0
	s_barrier
	s_add_u32 s8, s28, 0x40180
	s_addc_u32 s9, s29, 0
	s_add_i32 s60, s60, s38
	v_lshl_add_u64 v[2:3], s[8:9], 0, v[154:155]
	s_mov_b32 m0, s60
	s_add_i32 s61, s60, 0x2000
	global_load_lds_dwordx4 v[2:3], off
	v_lshl_add_u64 v[2:3], s[8:9], 0, v[150:151]
	s_mov_b32 m0, s61
	s_nop 0
	global_load_lds_dwordx4 v[2:3], off
	s_waitcnt vmcnt(6)
	s_barrier
	s_setprio 1
	v_mfma_f32_16x16x128_f8f6f4 v[106:109], v[212:219], v[180:187], v[106:109]
	v_mfma_f32_16x16x128_f8f6f4 v[102:105], v[220:227], v[180:187], v[102:105]
	v_mfma_f32_16x16x128_f8f6f4 v[74:77], v[212:219], v[188:195], v[74:77]
	v_mfma_f32_16x16x128_f8f6f4 v[62:65], v[220:227], v[188:195], v[62:65]
	v_mfma_f32_16x16x128_f8f6f4 v[50:53], v[212:219], v[196:203], v[50:53]
	v_mfma_f32_16x16x128_f8f6f4 v[42:45], v[220:227], v[196:203], v[42:45]
	v_mfma_f32_16x16x128_f8f6f4 v[34:37], v[212:219], v[204:211], v[34:37]
	v_mfma_f32_16x16x128_f8f6f4 v[26:29], v[220:227], v[204:211], v[26:29]
	s_setprio 0
	s_add_u32 s8, s30, 0x40180
	s_addc_u32 s9, s31, 0
	s_add_u32 s62, s28, 0x200
	s_addc_u32 s63, s29, 0
	s_mov_b32 s64, 0
	s_barrier
.LBB0_215:
	ds_read_b128 v[10:13], v175
	ds_read_b128 v[14:17], v175 offset:1024
	ds_read_b128 v[166:169], v175 offset:2048
	ds_read_b128 v[170:173], v175 offset:3072
	s_add_u32 s28, s8, 0xfffc0080
	s_addc_u32 s29, s9, -1
	s_cmp_eq_u32 s64, 12
	s_cselect_b32 s31, s13, s29
	s_cselect_b32 s30, s21, s28
	s_cselect_b32 s29, s15, s63
	s_cselect_b32 s28, s51, s62
	s_mov_b32 m0, s52
	v_lshl_add_u64 v[2:3], s[8:9], 0, v[158:159]
	ds_read_b128 v[180:183], v176
	ds_read_b128 v[184:187], v176 offset:1024
	ds_read_b128 v[188:191], v176 offset:2048
	ds_read_b128 v[192:195], v176 offset:3072
	ds_read_b128 v[196:199], v176 offset:4096
	ds_read_b128 v[200:203], v176 offset:5120
	ds_read_b128 v[204:207], v176 offset:6144
	ds_read_b128 v[208:211], v176 offset:7168
	global_load_lds_dwordx4 v[2:3], off
	v_lshl_add_u64 v[2:3], s[8:9], 0, v[160:161]
	s_mov_b32 m0, s53
	s_nop 0
	global_load_lds_dwordx4 v[2:3], off
	ds_read_b128 v[212:215], v177
	ds_read_b128 v[216:219], v177 offset:1024
	ds_read_b128 v[220:223], v177 offset:2048
	ds_read_b128 v[224:227], v177 offset:3072
	s_waitcnt vmcnt(8) lgkmcnt(0)
	s_barrier
	s_setprio 1
	v_mfma_f32_16x16x128_f8f6f4 v[138:141], v[10:17], v[180:187], v[138:141]
	v_mfma_f32_16x16x128_f8f6f4 v[134:137], v[166:173], v[180:187], v[134:137]
	v_mfma_f32_16x16x128_f8f6f4 v[122:125], v[10:17], v[188:195], v[122:125]
	v_mfma_f32_16x16x128_f8f6f4 v[118:121], v[166:173], v[188:195], v[118:121]
	v_mfma_f32_16x16x128_f8f6f4 v[98:101], v[10:17], v[196:203], v[98:101]
	v_mfma_f32_16x16x128_f8f6f4 v[90:93], v[166:173], v[196:203], v[90:93]
	v_mfma_f32_16x16x128_f8f6f4 v[70:73], v[10:17], v[204:211], v[70:73]
	v_mfma_f32_16x16x128_f8f6f4 v[58:61], v[166:173], v[204:211], v[58:61]
	v_mfma_f32_16x16x128_f8f6f4 v[146:149], v[212:219], v[180:187], v[146:149]
	v_mfma_f32_16x16x128_f8f6f4 v[142:145], v[220:227], v[180:187], v[142:145]
	v_mfma_f32_16x16x128_f8f6f4 v[130:133], v[212:219], v[188:195], v[130:133]
	v_mfma_f32_16x16x128_f8f6f4 v[126:129], v[220:227], v[188:195], v[126:129]
	v_mfma_f32_16x16x128_f8f6f4 v[114:117], v[212:219], v[196:203], v[114:117]
	v_mfma_f32_16x16x128_f8f6f4 v[110:113], v[220:227], v[196:203], v[110:113]
	v_mfma_f32_16x16x128_f8f6f4 v[82:85], v[212:219], v[204:211], v[82:85]
	v_mfma_f32_16x16x128_f8f6f4 v[78:81], v[220:227], v[204:211], v[78:81]
	s_setprio 0
	s_barrier
	ds_read_b128 v[180:183], v176 offset:16384
	ds_read_b128 v[184:187], v176 offset:17408
	ds_read_b128 v[188:191], v176 offset:18432
	ds_read_b128 v[192:195], v176 offset:19456
	ds_read_b128 v[196:199], v176 offset:20480
	ds_read_b128 v[200:203], v176 offset:21504
	ds_read_b128 v[204:207], v176 offset:22528
	ds_read_b128 v[208:211], v176 offset:23552
	s_mov_b32 m0, s54
	v_lshl_add_u64 v[6:7], s[28:29], 0, v[154:155]
	global_load_lds_dwordx4 v[6:7], off
	v_lshl_add_u64 v[8:9], s[28:29], 0, v[150:151]
	s_mov_b32 m0, s55
	s_nop 0
	global_load_lds_dwordx4 v[8:9], off
	s_mov_b32 m0, s27
	v_lshl_add_u64 v[2:3], s[30:31], 0, v[156:157]
	global_load_lds_dwordx4 v[2:3], off
	v_lshl_add_u64 v[4:5], s[30:31], 0, v[152:153]
	s_mov_b32 m0, s41
	s_nop 0
	global_load_lds_dwordx4 v[4:5], off
	s_add_u32 s66, s28, 0x40000
	s_addc_u32 s67, s29, 0
	s_mov_b32 m0, s56
	v_lshl_add_u64 v[228:229], s[66:67], 0, v[154:155]
	global_load_lds_dwordx4 v[228:229], off
	v_lshl_add_u64 v[228:229], s[66:67], 0, v[150:151]
	s_mov_b32 m0, s57
	s_nop 0
	global_load_lds_dwordx4 v[228:229], off
	s_waitcnt vmcnt(8) lgkmcnt(0)
	s_barrier
	s_setprio 1
	v_mfma_f32_16x16x128_f8f6f4 v[94:97], v[10:17], v[180:187], v[94:97]
	v_mfma_f32_16x16x128_f8f6f4 v[86:89], v[166:173], v[180:187], v[86:89]
	v_mfma_f32_16x16x128_f8f6f4 v[66:69], v[10:17], v[188:195], v[66:69]
	v_mfma_f32_16x16x128_f8f6f4 v[54:57], v[166:173], v[188:195], v[54:57]
	v_mfma_f32_16x16x128_f8f6f4 v[46:49], v[10:17], v[196:203], v[46:49]
	v_mfma_f32_16x16x128_f8f6f4 v[38:41], v[166:173], v[196:203], v[38:41]
	v_mfma_f32_16x16x128_f8f6f4 v[30:33], v[10:17], v[204:211], v[30:33]
	v_mfma_f32_16x16x128_f8f6f4 v[22:25], v[166:173], v[204:211], v[22:25]
	v_mfma_f32_16x16x128_f8f6f4 v[106:109], v[212:219], v[180:187], v[106:109]
	v_mfma_f32_16x16x128_f8f6f4 v[102:105], v[220:227], v[180:187], v[102:105]
	v_mfma_f32_16x16x128_f8f6f4 v[74:77], v[212:219], v[188:195], v[74:77]
	v_mfma_f32_16x16x128_f8f6f4 v[62:65], v[220:227], v[188:195], v[62:65]
	v_mfma_f32_16x16x128_f8f6f4 v[50:53], v[212:219], v[196:203], v[50:53]
	v_mfma_f32_16x16x128_f8f6f4 v[42:45], v[220:227], v[196:203], v[42:45]
	v_mfma_f32_16x16x128_f8f6f4 v[34:37], v[212:219], v[204:211], v[34:37]
	v_mfma_f32_16x16x128_f8f6f4 v[26:29], v[220:227], v[204:211], v[26:29]
	s_setprio 0
	s_barrier
	ds_read_b128 v[10:13], v178
	ds_read_b128 v[14:17], v178 offset:1024
	ds_read_b128 v[166:169], v178 offset:2048
	ds_read_b128 v[170:173], v178 offset:3072
	s_add_u32 s30, s30, 0x40000
	s_addc_u32 s31, s31, 0
	s_mov_b32 m0, s42
	v_lshl_add_u64 v[212:213], s[30:31], 0, v[156:157]
	ds_read_b128 v[180:183], v176 offset:32768
	ds_read_b128 v[184:187], v176 offset:33792
	ds_read_b128 v[188:191], v176 offset:34816
	ds_read_b128 v[192:195], v176 offset:35840
	ds_read_b128 v[196:199], v176 offset:36864
	ds_read_b128 v[200:203], v176 offset:37888
	ds_read_b128 v[204:207], v176 offset:38912
	ds_read_b128 v[208:211], v176 offset:39936
	global_load_lds_dwordx4 v[212:213], off
	v_lshl_add_u64 v[212:213], s[30:31], 0, v[152:153]
	s_mov_b32 m0, s43
	s_nop 0
	global_load_lds_dwordx4 v[212:213], off
	ds_read_b128 v[212:215], v179
	ds_read_b128 v[216:219], v179 offset:1024
	ds_read_b128 v[220:223], v179 offset:2048
	ds_read_b128 v[224:227], v179 offset:3072
	s_waitcnt vmcnt(8) lgkmcnt(0)
	s_barrier
	s_setprio 1
	v_mfma_f32_16x16x128_f8f6f4 v[138:141], v[10:17], v[180:187], v[138:141]
	v_mfma_f32_16x16x128_f8f6f4 v[134:137], v[166:173], v[180:187], v[134:137]
	v_mfma_f32_16x16x128_f8f6f4 v[122:125], v[10:17], v[188:195], v[122:125]
	v_mfma_f32_16x16x128_f8f6f4 v[118:121], v[166:173], v[188:195], v[118:121]
	v_mfma_f32_16x16x128_f8f6f4 v[98:101], v[10:17], v[196:203], v[98:101]
	v_mfma_f32_16x16x128_f8f6f4 v[90:93], v[166:173], v[196:203], v[90:93]
	v_mfma_f32_16x16x128_f8f6f4 v[70:73], v[10:17], v[204:211], v[70:73]
	v_mfma_f32_16x16x128_f8f6f4 v[58:61], v[166:173], v[204:211], v[58:61]
	v_mfma_f32_16x16x128_f8f6f4 v[146:149], v[212:219], v[180:187], v[146:149]
	v_mfma_f32_16x16x128_f8f6f4 v[142:145], v[220:227], v[180:187], v[142:145]
	v_mfma_f32_16x16x128_f8f6f4 v[130:133], v[212:219], v[188:195], v[130:133]
	v_mfma_f32_16x16x128_f8f6f4 v[126:129], v[220:227], v[188:195], v[126:129]
	v_mfma_f32_16x16x128_f8f6f4 v[114:117], v[212:219], v[196:203], v[114:117]
	v_mfma_f32_16x16x128_f8f6f4 v[110:113], v[220:227], v[196:203], v[110:113]
	v_mfma_f32_16x16x128_f8f6f4 v[82:85], v[212:219], v[204:211], v[82:85]
	v_mfma_f32_16x16x128_f8f6f4 v[78:81], v[220:227], v[204:211], v[78:81]
	s_setprio 0
	s_barrier
	ds_read_b128 v[180:183], v176 offset:49152
	ds_read_b128 v[184:187], v176 offset:50176
	ds_read_b128 v[188:191], v176 offset:51200
	ds_read_b128 v[192:195], v176 offset:52224
	ds_read_b128 v[196:199], v176 offset:53248
	ds_read_b128 v[200:203], v176 offset:54272
	ds_read_b128 v[204:207], v176 offset:55296
	ds_read_b128 v[208:211], v176 offset:56320
	s_mov_b32 m0, s58
	v_lshl_add_u64 v[6:7], v[6:7], 0, s[4:5]
	global_load_lds_dwordx4 v[6:7], off
	v_lshl_add_u64 v[6:7], v[8:9], 0, s[4:5]
	s_mov_b32 m0, s59
	s_nop 0
	global_load_lds_dwordx4 v[6:7], off
	s_mov_b32 m0, s44
	v_lshl_add_u64 v[2:3], v[2:3], 0, s[4:5]
	global_load_lds_dwordx4 v[2:3], off
	v_lshl_add_u64 v[2:3], v[4:5], 0, s[4:5]
	s_mov_b32 m0, s45
	s_nop 0
	global_load_lds_dwordx4 v[2:3], off
	s_add_u32 s28, s28, 0x40080
	s_addc_u32 s29, s29, 0
	s_mov_b32 m0, s60
	v_lshl_add_u64 v[2:3], s[28:29], 0, v[154:155]
	global_load_lds_dwordx4 v[2:3], off
	v_lshl_add_u64 v[2:3], s[28:29], 0, v[150:151]
	s_mov_b32 m0, s61
	s_nop 0
	global_load_lds_dwordx4 v[2:3], off
	s_waitcnt vmcnt(8) lgkmcnt(0)
	s_barrier
	s_setprio 1
	v_mfma_f32_16x16x128_f8f6f4 v[94:97], v[10:17], v[180:187], v[94:97]
	v_mfma_f32_16x16x128_f8f6f4 v[86:89], v[166:173], v[180:187], v[86:89]
	v_mfma_f32_16x16x128_f8f6f4 v[66:69], v[10:17], v[188:195], v[66:69]
	v_mfma_f32_16x16x128_f8f6f4 v[54:57], v[166:173], v[188:195], v[54:57]
	v_mfma_f32_16x16x128_f8f6f4 v[46:49], v[10:17], v[196:203], v[46:49]
	v_mfma_f32_16x16x128_f8f6f4 v[38:41], v[166:173], v[196:203], v[38:41]
	v_mfma_f32_16x16x128_f8f6f4 v[30:33], v[10:17], v[204:211], v[30:33]
	v_mfma_f32_16x16x128_f8f6f4 v[22:25], v[166:173], v[204:211], v[22:25]
	v_mfma_f32_16x16x128_f8f6f4 v[106:109], v[212:219], v[180:187], v[106:109]
	v_mfma_f32_16x16x128_f8f6f4 v[102:105], v[220:227], v[180:187], v[102:105]
	v_mfma_f32_16x16x128_f8f6f4 v[74:77], v[212:219], v[188:195], v[74:77]
	v_mfma_f32_16x16x128_f8f6f4 v[62:65], v[220:227], v[188:195], v[62:65]
	v_mfma_f32_16x16x128_f8f6f4 v[50:53], v[212:219], v[196:203], v[50:53]
	v_mfma_f32_16x16x128_f8f6f4 v[42:45], v[220:227], v[196:203], v[42:45]
	v_mfma_f32_16x16x128_f8f6f4 v[34:37], v[212:219], v[204:211], v[34:37]
	v_mfma_f32_16x16x128_f8f6f4 v[26:29], v[220:227], v[204:211], v[26:29]
	s_setprio 0
	s_add_i32 s64, s64, 2
	s_add_u32 s8, s8, 0x100
	s_addc_u32 s9, s9, 0
	s_add_u32 s62, s62, 0x100
	s_addc_u32 s63, s63, 0
	s_cmp_gt_u32 s64, 13
	s_barrier
	s_cbranch_scc0 .LBB0_215
	v_mov_b32_e32 v166, v0
	s_nop 15
	s_nop 15
	s_lshl_b32 s9, s26, 8
	v_readfirstlane_b32 s8, v166
	s_ashr_i32 s13, s8, 2
	s_andn2_b32 s13, s13, 63
	s_lshr_b32 s8, s8, 1
	s_add_i32 s13, s13, s9
	s_and_b32 s8, s8, 0x60
	s_lshl_b32 s9, s50, 8
	v_and_or_b32 v178, v166, 15, s13
	v_lshrrev_b32_e32 v166, 1, v166
	s_or_b32 s8, s8, s9
	v_and_or_b32 v168, v166, 24, s8
	v_mov_b64_e32 v[14:15], v[18:19]
	v_mov_b64_e32 v[10:11], v[18:19]
	v_mov_b64_e32 v[6:7], v[18:19]
	v_mov_b64_e32 v[2:3], v[18:19]
	v_ashrrev_i32_e32 v169, 31, v168
	v_mov_b64_e32 v[166:167], s[2:3]
	v_mov_b64_e32 v[16:17], v[20:21]
	v_mov_b64_e32 v[12:13], v[20:21]
	v_mov_b64_e32 v[8:9], v[20:21]
	v_mov_b64_e32 v[4:5], v[20:21]
	v_mad_i64_i32 v[170:171], s[8:9], v178, s49, v[166:167]
	v_lshlrev_b64 v[168:169], 1, v[168:169]
	s_waitcnt vmcnt(6)
	v_lshl_add_u64 v[170:171], v[170:171], 0, v[168:169]
	v_pk_fma_f32 v[140:141], v[140:141], s[18:19], v[16:17] op_sel_hi:[1,0,1]
	v_pk_fma_f32 v[138:139], v[138:139], s[18:19], v[14:15] op_sel_hi:[1,0,1]
	v_pk_fma_f32 v[172:173], v[136:137], s[18:19], v[12:13] op_sel_hi:[1,0,1]
	v_pk_fma_f32 v[136:137], v[134:135], s[18:19], v[10:11] op_sel_hi:[1,0,1]
	v_cvt_pk_bf16_f32 v134, v138, v139
	v_cvt_pk_bf16_f32 v135, v140, v141
	v_pk_fma_f32 v[138:139], v[144:145], s[18:19], v[4:5] op_sel_hi:[1,0,1]
	v_cvt_pk_bf16_f32 v136, v136, v137
	v_cvt_pk_bf16_f32 v137, v172, v173
	global_store_dwordx4 v[170:171], v[134:137], off
	v_pk_fma_f32 v[140:141], v[142:143], s[18:19], v[2:3] op_sel_hi:[1,0,1]
	v_pk_fma_f32 v[124:125], v[124:125], s[18:19], v[16:17] op_sel_hi:[1,0,1]
	v_pk_fma_f32 v[134:135], v[146:147], s[18:19], v[6:7] op_sel_hi:[1,0,1]
	v_pk_fma_f32 v[136:137], v[148:149], s[18:19], v[8:9] op_sel_hi:[1,0,1]
	v_cvt_pk_bf16_f32 v134, v134, v135
	v_pk_fma_f32 v[122:123], v[122:123], s[18:19], v[14:15] op_sel_hi:[1,0,1]
	v_cvt_pk_bf16_f32 v135, v136, v137
	v_cvt_pk_bf16_f32 v136, v140, v141
	v_cvt_pk_bf16_f32 v137, v138, v139
	global_store_dwordx4 v[170:171], v[134:137], off offset:256
	v_pk_fma_f32 v[100:101], v[100:101], s[18:19], v[16:17] op_sel_hi:[1,0,1]
	v_pk_fma_f32 v[98:99], v[98:99], s[18:19], v[14:15] op_sel_hi:[1,0,1]
	v_or_b32_e32 v134, 16, v178
	v_mad_i64_i32 v[134:135], s[8:9], v134, s49, v[166:167]
	v_lshl_add_u64 v[134:135], v[134:135], 0, v[168:169]
	v_pk_fma_f32 v[136:137], v[120:121], s[18:19], v[12:13] op_sel_hi:[1,0,1]
	v_pk_fma_f32 v[120:121], v[118:119], s[18:19], v[10:11] op_sel_hi:[1,0,1]
	v_cvt_pk_bf16_f32 v118, v122, v123
	v_cvt_pk_bf16_f32 v119, v124, v125
	v_pk_fma_f32 v[122:123], v[128:129], s[18:19], v[4:5] op_sel_hi:[1,0,1]
	v_cvt_pk_bf16_f32 v120, v120, v121
	v_cvt_pk_bf16_f32 v121, v136, v137
	global_store_dwordx4 v[134:135], v[118:121], off
	v_pk_fma_f32 v[124:125], v[126:127], s[18:19], v[2:3] op_sel_hi:[1,0,1]
	v_pk_fma_f32 v[72:73], v[72:73], s[18:19], v[16:17] op_sel_hi:[1,0,1]
	v_pk_fma_f32 v[118:119], v[130:131], s[18:19], v[6:7] op_sel_hi:[1,0,1]
	v_pk_fma_f32 v[120:121], v[132:133], s[18:19], v[8:9] op_sel_hi:[1,0,1]
	v_cvt_pk_bf16_f32 v118, v118, v119
	v_pk_fma_f32 v[70:71], v[70:71], s[18:19], v[14:15] op_sel_hi:[1,0,1]
	v_cvt_pk_bf16_f32 v119, v120, v121
	v_cvt_pk_bf16_f32 v120, v124, v125
	v_cvt_pk_bf16_f32 v121, v122, v123
	global_store_dwordx4 v[134:135], v[118:121], off offset:256
	v_pk_fma_f32 v[66:67], v[66:67], s[18:19], v[14:15] op_sel_hi:[1,0,1]
	v_pk_fma_f32 v[62:63], v[62:63], s[18:19], v[2:3] op_sel_hi:[1,0,1]
	v_or_b32_e32 v118, 32, v178
	v_mad_i64_i32 v[118:119], s[8:9], v118, s49, v[166:167]
	v_lshl_add_u64 v[118:119], v[118:119], 0, v[168:169]
	v_pk_fma_f32 v[120:121], v[92:93], s[18:19], v[12:13] op_sel_hi:[1,0,1]
	v_pk_fma_f32 v[92:93], v[90:91], s[18:19], v[10:11] op_sel_hi:[1,0,1]
	v_cvt_pk_bf16_f32 v90, v98, v99
	v_cvt_pk_bf16_f32 v91, v100, v101
	v_pk_fma_f32 v[98:99], v[112:113], s[18:19], v[4:5] op_sel_hi:[1,0,1]
	v_cvt_pk_bf16_f32 v92, v92, v93
	v_cvt_pk_bf16_f32 v93, v120, v121
	global_store_dwordx4 v[118:119], v[90:93], off
	v_pk_fma_f32 v[100:101], v[110:111], s[18:19], v[2:3] op_sel_hi:[1,0,1]
	v_pk_fma_f32 v[48:49], v[48:49], s[18:19], v[16:17] op_sel_hi:[1,0,1]
	v_pk_fma_f32 v[90:91], v[114:115], s[18:19], v[6:7] op_sel_hi:[1,0,1]
	v_pk_fma_f32 v[92:93], v[116:117], s[18:19], v[8:9] op_sel_hi:[1,0,1]
	v_cvt_pk_bf16_f32 v90, v90, v91
	v_pk_fma_f32 v[46:47], v[46:47], s[18:19], v[14:15] op_sel_hi:[1,0,1]
	v_cvt_pk_bf16_f32 v91, v92, v93
	v_cvt_pk_bf16_f32 v92, v100, v101
	v_cvt_pk_bf16_f32 v93, v98, v99
	global_store_dwordx4 v[118:119], v[90:93], off offset:256
	v_pk_fma_f32 v[44:45], v[44:45], s[18:19], v[4:5] op_sel_hi:[1,0,1]
	v_pk_fma_f32 v[42:43], v[42:43], s[18:19], v[2:3] op_sel_hi:[1,0,1]
	v_or_b32_e32 v90, 48, v178
	v_mad_i64_i32 v[90:91], s[8:9], v90, s49, v[166:167]
	v_lshl_add_u64 v[90:91], v[90:91], 0, v[168:169]
	v_pk_fma_f32 v[92:93], v[60:61], s[18:19], v[12:13] op_sel_hi:[1,0,1]
	v_pk_fma_f32 v[60:61], v[58:59], s[18:19], v[10:11] op_sel_hi:[1,0,1]
	v_cvt_pk_bf16_f32 v58, v70, v71
	v_cvt_pk_bf16_f32 v59, v72, v73
	v_pk_fma_f32 v[70:71], v[80:81], s[18:19], v[4:5] op_sel_hi:[1,0,1]
	v_cvt_pk_bf16_f32 v60, v60, v61
	v_cvt_pk_bf16_f32 v61, v92, v93
	global_store_dwordx4 v[90:91], v[58:61], off
	v_pk_fma_f32 v[72:73], v[78:79], s[18:19], v[2:3] op_sel_hi:[1,0,1]
	v_pk_fma_f32 v[78:79], v[86:87], s[18:19], v[10:11] op_sel_hi:[1,0,1]
	v_pk_fma_f32 v[58:59], v[82:83], s[18:19], v[6:7] op_sel_hi:[1,0,1]
	v_pk_fma_f32 v[60:61], v[84:85], s[18:19], v[8:9] op_sel_hi:[1,0,1]
	v_cvt_pk_bf16_f32 v58, v58, v59
	v_pk_fma_f32 v[24:25], v[24:25], s[18:19], v[12:13] op_sel_hi:[1,0,1]
	v_cvt_pk_bf16_f32 v59, v60, v61
	v_cvt_pk_bf16_f32 v60, v72, v73
	v_cvt_pk_bf16_f32 v61, v70, v71
	global_store_dwordx4 v[90:91], v[58:61], off offset:256
	v_pk_fma_f32 v[72:73], v[88:89], s[18:19], v[12:13] op_sel_hi:[1,0,1]
	s_and_b64 vcc, exec, s[6:7]
	v_add_u32_e32 v58, 0x80, v178
	v_mad_i64_i32 v[58:59], s[8:9], v58, s49, v[166:167]
	v_lshl_add_u64 v[70:71], v[58:59], 0, v[168:169]
	v_pk_fma_f32 v[58:59], v[94:95], s[18:19], v[14:15] op_sel_hi:[1,0,1]
	v_pk_fma_f32 v[60:61], v[96:97], s[18:19], v[16:17] op_sel_hi:[1,0,1]
	v_cvt_pk_bf16_f32 v58, v58, v59
	v_pk_fma_f32 v[14:15], v[30:31], s[18:19], v[14:15] op_sel_hi:[1,0,1]
	v_cvt_pk_bf16_f32 v59, v60, v61
	v_cvt_pk_bf16_f32 v60, v78, v79
	v_cvt_pk_bf16_f32 v61, v72, v73
	global_store_dwordx4 v[70:71], v[58:61], off
	v_pk_fma_f32 v[72:73], v[104:105], s[18:19], v[4:5] op_sel_hi:[1,0,1]
	v_pk_fma_f32 v[78:79], v[102:103], s[18:19], v[2:3] op_sel_hi:[1,0,1]
	v_pk_fma_f32 v[58:59], v[106:107], s[18:19], v[6:7] op_sel_hi:[1,0,1]
	v_pk_fma_f32 v[60:61], v[108:109], s[18:19], v[8:9] op_sel_hi:[1,0,1]
	v_cvt_pk_bf16_f32 v58, v58, v59
	s_mov_b32 s50, s14
	v_cvt_pk_bf16_f32 v59, v60, v61
	v_cvt_pk_bf16_f32 v60, v78, v79
	v_cvt_pk_bf16_f32 v61, v72, v73
	global_store_dwordx4 v[70:71], v[58:61], off offset:256
	s_mov_b32 s26, s20
	s_mov_b64 s[28:29], s[24:25]
	v_add_u32_e32 v58, 0x90, v178
	v_mad_i64_i32 v[58:59], s[8:9], v58, s49, v[166:167]
	v_lshl_add_u64 v[58:59], v[58:59], 0, v[168:169]
	v_pk_fma_f32 v[60:61], v[68:69], s[18:19], v[16:17] op_sel_hi:[1,0,1]
	v_pk_fma_f32 v[68:69], v[56:57], s[18:19], v[12:13] op_sel_hi:[1,0,1]
	v_pk_fma_f32 v[56:57], v[54:55], s[18:19], v[10:11] op_sel_hi:[1,0,1]
	v_cvt_pk_bf16_f32 v54, v66, v67
	v_cvt_pk_bf16_f32 v55, v60, v61
	v_pk_fma_f32 v[60:61], v[64:65], s[18:19], v[4:5] op_sel_hi:[1,0,1]
	v_cvt_pk_bf16_f32 v56, v56, v57
	v_cvt_pk_bf16_f32 v57, v68, v69
	global_store_dwordx4 v[58:59], v[54:57], off
	v_pk_fma_f32 v[16:17], v[32:33], s[18:19], v[16:17] op_sel_hi:[1,0,1]
	s_mov_b64 s[30:31], s[22:23]
	v_pk_fma_f32 v[54:55], v[74:75], s[18:19], v[6:7] op_sel_hi:[1,0,1]
	v_pk_fma_f32 v[56:57], v[76:77], s[18:19], v[8:9] op_sel_hi:[1,0,1]
	v_cvt_pk_bf16_f32 v54, v54, v55
	v_readlane_b32 s72, v254, 51
	v_cvt_pk_bf16_f32 v55, v56, v57
	v_cvt_pk_bf16_f32 v56, v62, v63
	v_cvt_pk_bf16_f32 v57, v60, v61
	global_store_dwordx4 v[58:59], v[54:57], off offset:256
	v_readlane_b32 s73, v254, 52
	s_nop 0
	v_add_u32_e32 v54, 0xa0, v178
	v_mad_i64_i32 v[54:55], s[8:9], v54, s49, v[166:167]
	v_lshl_add_u64 v[54:55], v[54:55], 0, v[168:169]
	v_pk_fma_f32 v[56:57], v[40:41], s[18:19], v[12:13] op_sel_hi:[1,0,1]
	v_pk_fma_f32 v[40:41], v[38:39], s[18:19], v[10:11] op_sel_hi:[1,0,1]
	v_cvt_pk_bf16_f32 v38, v46, v47
	v_cvt_pk_bf16_f32 v39, v48, v49
	v_pk_fma_f32 v[12:13], v[22:23], s[18:19], v[10:11] op_sel_hi:[1,0,1]
	v_cvt_pk_bf16_f32 v40, v40, v41
	v_cvt_pk_bf16_f32 v41, v56, v57
	global_store_dwordx4 v[54:55], v[38:41], off
	s_nop 1
	v_pk_fma_f32 v[38:39], v[50:51], s[18:19], v[6:7] op_sel_hi:[1,0,1]
	v_pk_fma_f32 v[40:41], v[52:53], s[18:19], v[8:9] op_sel_hi:[1,0,1]
	v_cvt_pk_bf16_f32 v38, v38, v39
	v_pk_fma_f32 v[8:9], v[36:37], s[18:19], v[8:9] op_sel_hi:[1,0,1]
	v_cvt_pk_bf16_f32 v39, v40, v41
	v_cvt_pk_bf16_f32 v40, v42, v43
	v_cvt_pk_bf16_f32 v41, v44, v45
	global_store_dwordx4 v[54:55], v[38:41], off offset:256
	v_cvt_pk_bf16_f32 v10, v14, v15
	v_cvt_pk_bf16_f32 v11, v16, v17
	v_cvt_pk_bf16_f32 v12, v12, v13
	v_cvt_pk_bf16_f32 v13, v24, v25
	v_pk_fma_f32 v[6:7], v[34:35], s[18:19], v[6:7] op_sel_hi:[1,0,1]
	s_nop 0
	v_add_u32_e32 v38, 0xb0, v178
	v_mad_i64_i32 v[38:39], s[8:9], v38, s49, v[166:167]
	v_lshl_add_u64 v[38:39], v[38:39], 0, v[168:169]
	global_store_dwordx4 v[38:39], v[10:13], off
	s_nop 1
	v_pk_fma_f32 v[10:11], v[28:29], s[18:19], v[4:5] op_sel_hi:[1,0,1]
	v_pk_fma_f32 v[4:5], v[26:27], s[18:19], v[2:3] op_sel_hi:[1,0,1]
	v_cvt_pk_bf16_f32 v2, v6, v7
	v_cvt_pk_bf16_f32 v3, v8, v9
	s_nop 0
	v_cvt_pk_bf16_f32 v4, v4, v5
	v_cvt_pk_bf16_f32 v5, v10, v11
	global_store_dwordx4 v[38:39], v[2:5], off offset:256
	s_cbranch_vccz .LBB0_212
	s_waitcnt vmcnt(0)
	v_readlane_b32 s44, v254, 43
	v_readlane_b32 s45, v254, 44
	s_cmpk_gt_u32 s19, 0xff
	s_mov_b64 s[52:53], s[44:45]
	v_readlane_b32 s46, v254, 45
	v_readlane_b32 s47, v254, 46
	s_cbranch_scc1 .LBB0_219
	s_barrier

.LBB0_714:
	v_readlane_b32 s2, v254, 60
	s_min_i32 s2, s18, s2
	s_sub_i32 s2, s10, s2
	s_ashr_i32 s30, s2, 3
	s_ashr_i32 s68, s28, 6
	s_sub_i32 s65, 0x7f, s30
	s_waitcnt vmcnt(45)
	v_and_b32_e32 v191, 7, v184
	s_lshl_b32 s67, s68, 3
	s_bfe_u32 s26, s2, 0x20001
	s_and_b32 s71, s2, 1
	s_lshl_b32 s66, s65, 6
	v_or_b32_e32 v205, s67, v191
	v_readlane_b32 s2, v254, 62
	v_bfe_u32 v2, v184, 3, 2
	v_add_u32_e32 v185, s66, v205
	s_lshl_b32 s94, s26, 13
	v_readlane_b32 s3, v254, 63
	s_waitcnt vmcnt(22)
	v_lshl_or_b32 v8, s71, 2, v2
	v_add_u32_e32 v2, s94, v185
	v_mov_b64_e32 v[4:5], s[2:3]
	v_bfe_u32 v190, v184, 5, 1
	v_mad_i64_i32 v[4:5], s[2:3], v2, s76, v[4:5]
	v_lshlrev_b32_e32 v2, 8, v8
	v_lshl_add_u64 v[6:7], v[4:5], 0, v[2:3]
	v_lshlrev_b32_e32 v138, 4, v190
	v_mov_b32_e32 v139, v3
	v_lshl_add_u64 v[6:7], v[6:7], 0, v[138:139]
	global_load_dwordx4 v[10:13], v[6:7], off
	s_mov_b64 s[2:3], 0x2c00
	global_load_dwordx4 v[140:143], v[6:7], off offset:32
	global_load_dwordx4 v[144:147], v[6:7], off offset:64
	global_load_dwordx4 v[148:151], v[6:7], off offset:96
	global_load_dwordx4 v[152:155], v[6:7], off offset:128
	global_load_dwordx4 v[156:159], v[6:7], off offset:160
	global_load_dwordx4 v[160:163], v[6:7], off offset:192
	global_load_dwordx4 v[164:167], v[6:7], off offset:224
	s_waitcnt vmcnt(0)
	v_lshlrev_b32_e32 v2, 16, v10
	v_and_b32_e32 v9, 0xffff0000, v10
	v_mul_f32_e32 v2, 0x3e0293ee, v2
	v_mul_f32_e32 v9, 0x3e0293ee, v9
	v_cvt_pk_bf16_f32 v100, v2, v9
	v_lshlrev_b32_e32 v2, 16, v11
	v_and_b32_e32 v9, 0xffff0000, v11
	v_mul_f32_e32 v2, 0x3e0293ee, v2
	v_mul_f32_e32 v9, 0x3e0293ee, v9
	v_cvt_pk_bf16_f32 v101, v2, v9
	v_lshlrev_b32_e32 v2, 16, v12
	v_and_b32_e32 v9, 0xffff0000, v12
	v_mul_f32_e32 v2, 0x3e0293ee, v2
	v_mul_f32_e32 v9, 0x3e0293ee, v9
	v_cvt_pk_bf16_f32 v102, v2, v9
	v_lshlrev_b32_e32 v2, 16, v13
	v_and_b32_e32 v9, 0xffff0000, v13
	v_mul_f32_e32 v2, 0x3e0293ee, v2
	v_mul_f32_e32 v9, 0x3e0293ee, v9
	v_cvt_pk_bf16_f32 v103, v2, v9
	v_lshlrev_b32_e32 v2, 16, v140
	v_and_b32_e32 v9, 0xffff0000, v140
	v_mul_f32_e32 v2, 0x3e0293ee, v2
	v_mul_f32_e32 v9, 0x3e0293ee, v9
	v_cvt_pk_bf16_f32 v104, v2, v9
	v_lshlrev_b32_e32 v2, 16, v141
	v_and_b32_e32 v9, 0xffff0000, v141
	v_mul_f32_e32 v2, 0x3e0293ee, v2
	v_mul_f32_e32 v9, 0x3e0293ee, v9
	v_cvt_pk_bf16_f32 v105, v2, v9
	v_lshlrev_b32_e32 v2, 16, v142
	v_and_b32_e32 v9, 0xffff0000, v142
	v_mul_f32_e32 v2, 0x3e0293ee, v2
	v_mul_f32_e32 v9, 0x3e0293ee, v9
	v_cvt_pk_bf16_f32 v106, v2, v9
	v_lshlrev_b32_e32 v2, 16, v143
	v_and_b32_e32 v9, 0xffff0000, v143
	v_mul_f32_e32 v2, 0x3e0293ee, v2
	v_mul_f32_e32 v9, 0x3e0293ee, v9
	v_cvt_pk_bf16_f32 v107, v2, v9
	v_lshlrev_b32_e32 v2, 16, v144
	v_and_b32_e32 v9, 0xffff0000, v144
	v_mul_f32_e32 v2, 0x3e0293ee, v2
	v_mul_f32_e32 v9, 0x3e0293ee, v9
	v_cvt_pk_bf16_f32 v108, v2, v9
	v_lshlrev_b32_e32 v2, 16, v145
	v_and_b32_e32 v9, 0xffff0000, v145
	v_mul_f32_e32 v2, 0x3e0293ee, v2
	v_mul_f32_e32 v9, 0x3e0293ee, v9
	v_cvt_pk_bf16_f32 v109, v2, v9
	v_lshlrev_b32_e32 v2, 16, v146
	v_and_b32_e32 v9, 0xffff0000, v146
	v_mul_f32_e32 v2, 0x3e0293ee, v2
	v_mul_f32_e32 v9, 0x3e0293ee, v9
	v_cvt_pk_bf16_f32 v110, v2, v9
	v_lshlrev_b32_e32 v2, 16, v147
	v_and_b32_e32 v9, 0xffff0000, v147
	v_mul_f32_e32 v2, 0x3e0293ee, v2
	v_mul_f32_e32 v9, 0x3e0293ee, v9
	v_cvt_pk_bf16_f32 v111, v2, v9
	v_lshlrev_b32_e32 v2, 16, v148
	v_and_b32_e32 v9, 0xffff0000, v148
	v_mul_f32_e32 v2, 0x3e0293ee, v2
	v_mul_f32_e32 v9, 0x3e0293ee, v9
	v_cvt_pk_bf16_f32 v112, v2, v9
	v_lshlrev_b32_e32 v2, 16, v149
	v_and_b32_e32 v9, 0xffff0000, v149
	v_mul_f32_e32 v2, 0x3e0293ee, v2
	v_mul_f32_e32 v9, 0x3e0293ee, v9
	v_cvt_pk_bf16_f32 v113, v2, v9
	v_lshlrev_b32_e32 v2, 16, v150
	v_and_b32_e32 v9, 0xffff0000, v150
	v_mul_f32_e32 v2, 0x3e0293ee, v2
	v_mul_f32_e32 v9, 0x3e0293ee, v9
	v_cvt_pk_bf16_f32 v114, v2, v9
	v_lshlrev_b32_e32 v2, 16, v151
	v_and_b32_e32 v9, 0xffff0000, v151
	v_mul_f32_e32 v2, 0x3e0293ee, v2
	v_mul_f32_e32 v9, 0x3e0293ee, v9
	v_cvt_pk_bf16_f32 v115, v2, v9
	v_lshlrev_b32_e32 v2, 16, v152
	v_and_b32_e32 v9, 0xffff0000, v152
	v_mul_f32_e32 v2, 0x3e0293ee, v2
	v_mul_f32_e32 v9, 0x3e0293ee, v9
	v_cvt_pk_bf16_f32 v116, v2, v9
	v_lshlrev_b32_e32 v2, 16, v153
	v_and_b32_e32 v9, 0xffff0000, v153
	v_mul_f32_e32 v2, 0x3e0293ee, v2
	v_mul_f32_e32 v9, 0x3e0293ee, v9
	v_cvt_pk_bf16_f32 v117, v2, v9
	v_lshlrev_b32_e32 v2, 16, v154
	v_and_b32_e32 v9, 0xffff0000, v154
	v_mul_f32_e32 v2, 0x3e0293ee, v2
	v_mul_f32_e32 v9, 0x3e0293ee, v9
	v_cvt_pk_bf16_f32 v118, v2, v9
	v_lshlrev_b32_e32 v2, 16, v155
	v_and_b32_e32 v9, 0xffff0000, v155
	v_mul_f32_e32 v2, 0x3e0293ee, v2
	v_mul_f32_e32 v9, 0x3e0293ee, v9
	v_cvt_pk_bf16_f32 v119, v2, v9
	v_lshlrev_b32_e32 v2, 16, v156
	v_and_b32_e32 v9, 0xffff0000, v156
	v_mul_f32_e32 v2, 0x3e0293ee, v2
	v_mul_f32_e32 v9, 0x3e0293ee, v9
	v_cvt_pk_bf16_f32 v120, v2, v9
	v_lshlrev_b32_e32 v2, 16, v157
	v_and_b32_e32 v9, 0xffff0000, v157
	v_mul_f32_e32 v2, 0x3e0293ee, v2
	v_mul_f32_e32 v9, 0x3e0293ee, v9
	v_cvt_pk_bf16_f32 v121, v2, v9
	v_lshlrev_b32_e32 v2, 16, v158
	v_and_b32_e32 v9, 0xffff0000, v158
	v_mul_f32_e32 v2, 0x3e0293ee, v2
	v_mul_f32_e32 v9, 0x3e0293ee, v9
	v_cvt_pk_bf16_f32 v122, v2, v9
	v_lshlrev_b32_e32 v2, 16, v159
	v_and_b32_e32 v9, 0xffff0000, v159
	v_mul_f32_e32 v2, 0x3e0293ee, v2
	v_mul_f32_e32 v9, 0x3e0293ee, v9
	v_cvt_pk_bf16_f32 v123, v2, v9
	v_lshlrev_b32_e32 v2, 16, v160
	v_and_b32_e32 v9, 0xffff0000, v160
	v_mul_f32_e32 v2, 0x3e0293ee, v2
	v_mul_f32_e32 v9, 0x3e0293ee, v9
	v_cvt_pk_bf16_f32 v124, v2, v9
	v_lshlrev_b32_e32 v2, 16, v161
	v_and_b32_e32 v9, 0xffff0000, v161
	v_mul_f32_e32 v2, 0x3e0293ee, v2
	v_mul_f32_e32 v9, 0x3e0293ee, v9
	v_cvt_pk_bf16_f32 v125, v2, v9
	v_lshlrev_b32_e32 v2, 16, v162
	v_and_b32_e32 v9, 0xffff0000, v162
	v_mul_f32_e32 v2, 0x3e0293ee, v2
	v_mul_f32_e32 v9, 0x3e0293ee, v9
	v_cvt_pk_bf16_f32 v126, v2, v9
	v_lshlrev_b32_e32 v2, 16, v163
	v_and_b32_e32 v9, 0xffff0000, v163
	v_mul_f32_e32 v2, 0x3e0293ee, v2
	v_mul_f32_e32 v9, 0x3e0293ee, v9
	v_cvt_pk_bf16_f32 v127, v2, v9
	v_lshlrev_b32_e32 v2, 16, v164
	v_mul_f32_e32 v2, 0x3e0293ee, v2
	v_and_b32_e32 v6, 0xffff0000, v164
	v_mul_f32_e32 v6, 0x3e0293ee, v6
	v_cvt_pk_bf16_f32 v128, v2, v6
	v_lshlrev_b32_e32 v2, 16, v165
	v_mul_f32_e32 v2, 0x3e0293ee, v2
	v_and_b32_e32 v6, 0xffff0000, v165
	v_mul_f32_e32 v6, 0x3e0293ee, v6
	v_cvt_pk_bf16_f32 v129, v2, v6
	v_lshlrev_b32_e32 v2, 16, v166
	v_mul_f32_e32 v2, 0x3e0293ee, v2
	v_and_b32_e32 v6, 0xffff0000, v166
	v_mul_f32_e32 v6, 0x3e0293ee, v6
	v_cvt_pk_bf16_f32 v130, v2, v6
	v_lshlrev_b32_e32 v2, 16, v167
	v_mul_f32_e32 v2, 0x3e0293ee, v2
	v_and_b32_e32 v6, 0xffff0000, v167
	v_mul_f32_e32 v6, 0x3e0293ee, v6
	v_cvt_pk_bf16_f32 v131, v2, v6
	v_mul_u32_u24_e32 v2, 3, v8
	v_lshlrev_b32_e32 v2, 1, v2
	v_lshl_add_u64 v[4:5], v[4:5], 0, v[2:3]
	v_lshl_add_u64 v[6:7], v[4:5], 0, s[2:3]
	v_add_co_u32_e32 v4, vcc, 0x2000, v4
	s_movk_i32 s2, 0x2100
	s_nop 0
	v_addc_co_u32_e32 v5, vcc, 0, v5, vcc
	global_load_dword v204, v[4:5], off offset:3072
	global_load_ushort v186, v[6:7], off offset:4
	v_cmp_gt_i32_e32 vcc, s2, v184
	s_and_saveexec_b64 s[2:3], vcc
	s_cbranch_execz .LBB0_717
	v_readlane_b32 s6, v255, 10
	v_add_u32_e32 v2, 0xfffffe00, v184
	s_nop 0
	v_lshl_add_u32 v4, v184, 2, s6
	s_mov_b64 s[6:7], 0

.LBB0_1441:
	s_add_u32 s41, s35, s36
	ds_read_b128 v[2:5], v176
	ds_read_b128 v[6:9], v176 offset:1024
	ds_read_b128 v[10:13], v176 offset:2048
	ds_read_b128 v[14:17], v176 offset:3072
	s_addc_u32 s45, s53, s37
	s_ashr_i32 s39, s38, 31
	s_lshl_b64 s[6:7], s[38:39], 19
	s_add_u32 s6, s41, s6
	s_addc_u32 s7, s45, s7
	s_and_b64 s[48:49], s[42:43], exec
	s_cselect_b32 s39, s7, s47
	s_cselect_b32 s41, s6, s46
	s_add_i32 s45, s55, 0xc000
	s_mov_b32 m0, s45
	s_add_i32 s69, s55, 0xe000
	ds_read_b128 v[34:37], v177
	ds_read_b128 v[38:41], v177 offset:1024
	ds_read_b128 v[42:45], v177 offset:2048
	ds_read_b128 v[46:49], v177 offset:3072
	ds_read_b128 v[50:53], v177 offset:4096
	ds_read_b128 v[54:57], v177 offset:5120
	ds_read_b128 v[58:61], v177 offset:6144
	ds_read_b128 v[62:65], v177 offset:7168
	global_load_lds_dwordx4 v168, s[20:21]
	s_mov_b32 m0, s69
	v_mov_b32_e32 v169, v167
	global_load_lds_dwordx4 v170, s[20:21]
	s_waitcnt lgkmcnt(8)
	s_barrier
	s_waitcnt lgkmcnt(0)
	v_mov_b32_e32 v171, v167
	s_setprio 1
	s_waitcnt lgkmcnt(0)
	v_mfma_f32_16x16x128_f8f6f4 v[154:157], v[2:9], v[34:41], 0
	v_mfma_f32_16x16x128_f8f6f4 v[146:149], v[10:17], v[34:41], 0
	v_mfma_f32_16x16x128_f8f6f4 v[138:141], v[2:9], v[42:49], 0
	v_mfma_f32_16x16x128_f8f6f4 v[130:133], v[10:17], v[42:49], 0
	v_mfma_f32_16x16x128_f8f6f4 v[122:125], v[2:9], v[50:57], 0
	v_mfma_f32_16x16x128_f8f6f4 v[114:117], v[10:17], v[50:57], 0
	v_mfma_f32_16x16x128_f8f6f4 v[106:109], v[2:9], v[58:65], 0
	v_mfma_f32_16x16x128_f8f6f4 v[90:93], v[10:17], v[58:65], 0
	s_setprio 0
	s_barrier
	v_lshl_add_u64 v[236:237], s[46:47], 0, v[162:163]
	s_add_i32 s70, s63, s54
	v_lshl_add_u64 v[66:67], v[236:237], 0, s[26:27]
	s_mov_b32 m0, s70
	v_lshl_add_u64 v[238:239], s[46:47], 0, v[164:165]
	s_add_i32 s71, s70, 0x2000
	ds_read_b128 v[186:189], v178
	ds_read_b128 v[190:193], v178 offset:1024
	ds_read_b128 v[194:197], v178 offset:2048
	ds_read_b128 v[198:201], v178 offset:3072
	global_load_lds_dwordx4 v[66:67], off
	v_lshl_add_u64 v[66:67], v[238:239], 0, s[26:27]
	s_mov_b32 m0, s71
	s_nop 0
	global_load_lds_dwordx4 v[66:67], off
	s_barrier
	s_waitcnt lgkmcnt(0)
	s_setprio 1
	s_waitcnt lgkmcnt(0)
	v_mfma_f32_16x16x128_f8f6f4 v[158:161], v[186:193], v[34:41], 0
	v_mfma_f32_16x16x128_f8f6f4 v[150:153], v[194:201], v[34:41], 0
	v_mfma_f32_16x16x128_f8f6f4 v[142:145], v[186:193], v[42:49], 0
	v_mfma_f32_16x16x128_f8f6f4 v[134:137], v[194:201], v[42:49], 0
	v_mfma_f32_16x16x128_f8f6f4 v[126:129], v[186:193], v[50:57], 0
	v_mfma_f32_16x16x128_f8f6f4 v[118:121], v[194:201], v[50:57], 0
	v_mfma_f32_16x16x128_f8f6f4 v[110:113], v[186:193], v[58:65], 0
	v_mfma_f32_16x16x128_f8f6f4 v[98:101], v[194:201], v[58:65], 0
	s_setprio 0
	s_mov_b32 m0, s55
	s_barrier
	ds_read_b128 v[202:205], v177 offset:16384
	ds_read_b128 v[206:209], v177 offset:17408
	ds_read_b128 v[210:213], v177 offset:18432
	ds_read_b128 v[214:217], v177 offset:19456
	ds_read_b128 v[218:221], v177 offset:20480
	ds_read_b128 v[222:225], v177 offset:21504
	ds_read_b128 v[226:229], v177 offset:22528
	ds_read_b128 v[230:233], v177 offset:23552
	global_load_lds_dwordx4 v184, s[22:23]
	s_mov_b32 m0, s56
	s_nop 0
	global_load_lds_dwordx4 v172, s[22:23]
	s_barrier
	s_waitcnt lgkmcnt(0)
	s_setprio 1
	s_waitcnt lgkmcnt(0)
	v_mfma_f32_16x16x128_f8f6f4 v[94:97], v[2:9], v[202:209], 0
	v_mfma_f32_16x16x128_f8f6f4 v[82:85], v[10:17], v[202:209], 0
	v_mfma_f32_16x16x128_f8f6f4 v[74:77], v[2:9], v[210:217], 0
	v_mfma_f32_16x16x128_f8f6f4 v[66:69], v[10:17], v[210:217], 0
	v_mfma_f32_16x16x128_f8f6f4 v[58:61], v[2:9], v[218:225], 0
	v_mfma_f32_16x16x128_f8f6f4 v[50:53], v[10:17], v[218:225], 0
	v_mfma_f32_16x16x128_f8f6f4 v[42:45], v[2:9], v[226:233], 0
	v_mfma_f32_16x16x128_f8f6f4 v[34:37], v[10:17], v[226:233], 0
	s_setprio 0
	s_barrier
	s_add_u32 s48, s46, 0x40100
	s_addc_u32 s49, s47, 0
	s_add_i32 s72, s64, s54
	v_lshl_add_u64 v[2:3], s[48:49], 0, v[162:163]
	s_mov_b32 m0, s72
	s_add_i32 s73, s72, 0x2000
	global_load_lds_dwordx4 v[2:3], off
	v_lshl_add_u64 v[2:3], s[48:49], 0, v[164:165]
	s_mov_b32 m0, s73
	s_nop 0
	global_load_lds_dwordx4 v[2:3], off
	s_waitcnt vmcnt(6)
	s_barrier
	s_setprio 1
	v_mfma_f32_16x16x128_f8f6f4 v[102:105], v[186:193], v[202:209], 0
	v_mfma_f32_16x16x128_f8f6f4 v[86:89], v[194:201], v[202:209], 0
	v_mfma_f32_16x16x128_f8f6f4 v[78:81], v[186:193], v[210:217], 0
	v_mfma_f32_16x16x128_f8f6f4 v[70:73], v[194:201], v[210:217], 0
	v_mfma_f32_16x16x128_f8f6f4 v[62:65], v[186:193], v[218:225], 0
	v_mfma_f32_16x16x128_f8f6f4 v[54:57], v[194:201], v[218:225], 0
	v_mfma_f32_16x16x128_f8f6f4 v[46:49], v[186:193], v[226:233], 0
	v_mfma_f32_16x16x128_f8f6f4 v[38:41], v[194:201], v[226:233], 0
	s_setprio 0
	s_add_i32 s74, 0, 0x18000
	v_add_u32_e32 v185, s74, v173
	s_barrier
	ds_read_b128 v[2:5], v185
	ds_read_b128 v[6:9], v185 offset:1024
	ds_read_b128 v[10:13], v185 offset:2048
	ds_read_b128 v[14:17], v185 offset:3072
	s_mov_b32 m0, s57
	ds_read_b128 v[188:191], v177 offset:32768
	ds_read_b128 v[192:195], v177 offset:33792
	ds_read_b128 v[196:199], v177 offset:34816
	ds_read_b128 v[200:203], v177 offset:35840
	ds_read_b128 v[204:207], v177 offset:36864
	ds_read_b128 v[208:211], v177 offset:37888
	ds_read_b128 v[212:215], v177 offset:38912
	ds_read_b128 v[216:219], v177 offset:39936
	global_load_lds_dwordx4 v168, s[22:23]
	s_mov_b32 m0, s58
	s_nop 0
	global_load_lds_dwordx4 v170, s[22:23]
	s_waitcnt lgkmcnt(8)
	s_barrier
	s_waitcnt lgkmcnt(0)
	s_setprio 1
	s_waitcnt lgkmcnt(0)
	v_mfma_f32_16x16x128_f8f6f4 v[154:157], v[2:9], v[188:195], v[154:157]
	v_mfma_f32_16x16x128_f8f6f4 v[146:149], v[10:17], v[188:195], v[146:149]
	v_mfma_f32_16x16x128_f8f6f4 v[138:141], v[2:9], v[196:203], v[138:141]
	v_mfma_f32_16x16x128_f8f6f4 v[130:133], v[10:17], v[196:203], v[130:133]
	v_mfma_f32_16x16x128_f8f6f4 v[122:125], v[2:9], v[204:211], v[122:125]
	v_mfma_f32_16x16x128_f8f6f4 v[114:117], v[10:17], v[204:211], v[114:117]
	v_mfma_f32_16x16x128_f8f6f4 v[106:109], v[2:9], v[212:219], v[106:109]
	v_mfma_f32_16x16x128_f8f6f4 v[90:93], v[10:17], v[212:219], v[90:93]
	s_setprio 0
	s_barrier
	s_add_i32 s76, 0, 0x1c000
	s_add_i32 s74, s74, s54
	v_add_u32_e32 v186, s76, v173
	v_lshl_add_u64 v[236:237], v[236:237], 0, s[28:29]
	s_mov_b32 m0, s74
	s_add_i32 s75, s74, 0x2000
	ds_read_b128 v[220:223], v186
	ds_read_b128 v[224:227], v186 offset:1024
	ds_read_b128 v[228:231], v186 offset:2048
	ds_read_b128 v[232:235], v186 offset:3072
	global_load_lds_dwordx4 v[236:237], off
	v_lshl_add_u64 v[236:237], v[238:239], 0, s[28:29]
	s_mov_b32 m0, s75
	s_nop 0
	global_load_lds_dwordx4 v[236:237], off
	s_barrier
	s_waitcnt lgkmcnt(0)
	s_setprio 1
	s_waitcnt lgkmcnt(0)
	v_mfma_f32_16x16x128_f8f6f4 v[158:161], v[220:227], v[188:195], v[158:161]
	v_mfma_f32_16x16x128_f8f6f4 v[150:153], v[228:235], v[188:195], v[150:153]
	v_mfma_f32_16x16x128_f8f6f4 v[142:145], v[220:227], v[196:203], v[142:145]
	v_mfma_f32_16x16x128_f8f6f4 v[134:137], v[228:235], v[196:203], v[134:137]
	v_mfma_f32_16x16x128_f8f6f4 v[126:129], v[220:227], v[204:211], v[126:129]
	v_mfma_f32_16x16x128_f8f6f4 v[118:121], v[228:235], v[204:211], v[118:121]
	v_mfma_f32_16x16x128_f8f6f4 v[110:113], v[220:227], v[212:219], v[110:113]
	v_mfma_f32_16x16x128_f8f6f4 v[98:101], v[228:235], v[212:219], v[98:101]
	s_setprio 0
	s_mov_b32 m0, s60
	s_barrier
	ds_read_b128 v[188:191], v177 offset:49152
	ds_read_b128 v[192:195], v177 offset:50176
	ds_read_b128 v[196:199], v177 offset:51200
	ds_read_b128 v[200:203], v177 offset:52224
	ds_read_b128 v[204:207], v177 offset:53248
	ds_read_b128 v[208:211], v177 offset:54272
	ds_read_b128 v[212:215], v177 offset:55296
	ds_read_b128 v[216:219], v177 offset:56320
	global_load_lds_dwordx4 v184, s[24:25]
	s_mov_b32 m0, s61
	s_nop 0
	global_load_lds_dwordx4 v172, s[24:25]
	s_barrier
	s_waitcnt lgkmcnt(0)
	s_setprio 1
	s_waitcnt lgkmcnt(0)
	v_mfma_f32_16x16x128_f8f6f4 v[94:97], v[2:9], v[188:195], v[94:97]
	v_mfma_f32_16x16x128_f8f6f4 v[82:85], v[10:17], v[188:195], v[82:85]
	v_mfma_f32_16x16x128_f8f6f4 v[74:77], v[2:9], v[196:203], v[74:77]
	v_mfma_f32_16x16x128_f8f6f4 v[66:69], v[10:17], v[196:203], v[66:69]
	v_mfma_f32_16x16x128_f8f6f4 v[58:61], v[2:9], v[204:211], v[58:61]
	v_mfma_f32_16x16x128_f8f6f4 v[50:53], v[10:17], v[204:211], v[50:53]
	v_mfma_f32_16x16x128_f8f6f4 v[42:45], v[2:9], v[212:219], v[42:45]
	v_mfma_f32_16x16x128_f8f6f4 v[34:37], v[10:17], v[212:219], v[34:37]
	s_setprio 0
	s_barrier
	s_add_u32 s48, s46, 0x40180
	s_addc_u32 s49, s47, 0
	s_add_i32 s76, s76, s54
	v_lshl_add_u64 v[2:3], s[48:49], 0, v[162:163]
	s_mov_b32 m0, s76
	s_add_i32 s77, s76, 0x2000
	global_load_lds_dwordx4 v[2:3], off
	v_lshl_add_u64 v[2:3], s[48:49], 0, v[164:165]
	s_mov_b32 m0, s77
	s_nop 0
	global_load_lds_dwordx4 v[2:3], off
	s_waitcnt vmcnt(6)
	s_barrier
	s_setprio 1
	v_mfma_f32_16x16x128_f8f6f4 v[102:105], v[220:227], v[188:195], v[102:105]
	v_mfma_f32_16x16x128_f8f6f4 v[86:89], v[228:235], v[188:195], v[86:89]
	v_mfma_f32_16x16x128_f8f6f4 v[78:81], v[220:227], v[196:203], v[78:81]
	v_mfma_f32_16x16x128_f8f6f4 v[70:73], v[228:235], v[196:203], v[70:73]
	v_mfma_f32_16x16x128_f8f6f4 v[62:65], v[220:227], v[204:211], v[62:65]
	v_mfma_f32_16x16x128_f8f6f4 v[54:57], v[228:235], v[204:211], v[54:57]
	v_mfma_f32_16x16x128_f8f6f4 v[46:49], v[220:227], v[212:219], v[46:49]
	v_mfma_f32_16x16x128_f8f6f4 v[38:41], v[228:235], v[212:219], v[38:41]
	s_setprio 0
	s_add_u32 s78, s46, 0x200
	v_lshl_add_u64 v[2:3], s[24:25], 0, v[170:171]
	v_lshl_add_u64 v[4:5], s[24:25], 0, v[168:169]
	s_addc_u32 s79, s47, 0
	s_mov_b32 s80, 0
	s_mov_b64 s[46:47], 0
	s_barrier
.LBB0_1442:
	s_add_u32 s48, s96, s46
	s_addc_u32 s49, s97, s47
	s_add_u32 s50, s48, 0x32370200
	ds_read_b128 v[188:191], v176
	ds_read_b128 v[192:195], v176 offset:1024
	ds_read_b128 v[196:199], v176 offset:2048
	ds_read_b128 v[200:203], v176 offset:3072
	s_addc_u32 s51, s49, 0
	s_add_u32 s81, s78, s46
	s_addc_u32 s82, s79, s47
	s_cmpk_eq_i32 s46, 0x600
	s_cselect_b64 vcc, -1, 0
	s_and_b64 s[48:49], vcc, exec
	v_cndmask_b32_e32 v166, v184, v180, vcc
	s_cselect_b32 s51, s11, s51
	s_cselect_b32 s50, s10, s50
	v_cndmask_b32_e32 v252, v172, v182, vcc
	v_cndmask_b32_e32 v169, v168, v181, vcc
	v_cndmask_b32_e32 v171, v170, v183, vcc
	s_cselect_b32 s49, s39, s82
	s_cselect_b32 s48, s41, s81
	s_mov_b32 m0, s45
	v_lshl_add_u64 v[6:7], v[4:5], 0, s[46:47]
	ds_read_b128 v[10:13], v177
	ds_read_b128 v[14:17], v177 offset:1024
	ds_read_b128 v[204:207], v177 offset:2048
	ds_read_b128 v[208:211], v177 offset:3072
	ds_read_b128 v[212:215], v177 offset:4096
	ds_read_b128 v[216:219], v177 offset:5120
	ds_read_b128 v[220:223], v177 offset:6144
	ds_read_b128 v[224:227], v177 offset:7168
	global_load_lds_dwordx4 v[6:7], off
	v_lshl_add_u64 v[6:7], v[2:3], 0, s[46:47]
	s_mov_b32 m0, s69
	s_nop 0
	global_load_lds_dwordx4 v[6:7], off
	ds_read_b128 v[228:231], v178
	ds_read_b128 v[232:235], v178 offset:1024
	ds_read_b128 v[236:239], v178 offset:2048
	ds_read_b128 v[240:243], v178 offset:3072
	s_waitcnt vmcnt(8) lgkmcnt(0)
	s_barrier
	s_setprio 1
	v_mfma_f32_16x16x128_f8f6f4 v[154:157], v[188:195], v[10:17], v[154:157]
	v_mfma_f32_16x16x128_f8f6f4 v[146:149], v[196:203], v[10:17], v[146:149]
	v_mfma_f32_16x16x128_f8f6f4 v[138:141], v[188:195], v[204:211], v[138:141]
	v_mfma_f32_16x16x128_f8f6f4 v[130:133], v[196:203], v[204:211], v[130:133]
	v_mfma_f32_16x16x128_f8f6f4 v[122:125], v[188:195], v[212:219], v[122:125]
	v_mfma_f32_16x16x128_f8f6f4 v[114:117], v[196:203], v[212:219], v[114:117]
	v_mfma_f32_16x16x128_f8f6f4 v[106:109], v[188:195], v[220:227], v[106:109]
	v_mfma_f32_16x16x128_f8f6f4 v[90:93], v[196:203], v[220:227], v[90:93]
	v_mfma_f32_16x16x128_f8f6f4 v[158:161], v[228:235], v[10:17], v[158:161]
	v_mfma_f32_16x16x128_f8f6f4 v[150:153], v[236:243], v[10:17], v[150:153]
	v_mfma_f32_16x16x128_f8f6f4 v[142:145], v[228:235], v[204:211], v[142:145]
	v_mfma_f32_16x16x128_f8f6f4 v[134:137], v[236:243], v[204:211], v[134:137]
	v_mfma_f32_16x16x128_f8f6f4 v[126:129], v[228:235], v[212:219], v[126:129]
	v_mfma_f32_16x16x128_f8f6f4 v[118:121], v[236:243], v[212:219], v[118:121]
	v_mfma_f32_16x16x128_f8f6f4 v[110:113], v[228:235], v[220:227], v[110:113]
	v_mfma_f32_16x16x128_f8f6f4 v[98:101], v[236:243], v[220:227], v[98:101]
	s_setprio 0
	s_barrier
	ds_read_b128 v[204:207], v177 offset:16384
	ds_read_b128 v[208:211], v177 offset:17408
	ds_read_b128 v[212:215], v177 offset:18432
	ds_read_b128 v[216:219], v177 offset:19456
	ds_read_b128 v[220:223], v177 offset:20480
	ds_read_b128 v[224:227], v177 offset:21504
	ds_read_b128 v[244:247], v177 offset:22528
	ds_read_b128 v[248:251], v177 offset:23552
	s_mov_b32 m0, s70
	v_lshl_add_u64 v[6:7], s[48:49], 0, v[162:163]
	global_load_lds_dwordx4 v[6:7], off
	v_lshl_add_u64 v[8:9], s[48:49], 0, v[164:165]
	s_mov_b32 m0, s71
	s_nop 0
	global_load_lds_dwordx4 v[8:9], off
	s_mov_b32 m0, s55
	s_nop 0
	global_load_lds_dwordx4 v166, s[50:51]
	s_mov_b32 m0, s56
	v_mov_b32_e32 v253, v167
	global_load_lds_dwordx4 v252, s[50:51]
	s_add_u32 s82, s48, 0x40000
	s_addc_u32 s83, s49, 0
	s_mov_b32 m0, s72
	v_lshl_add_u64 v[14:15], s[82:83], 0, v[162:163]
	global_load_lds_dwordx4 v[14:15], off
	v_lshl_add_u64 v[14:15], s[82:83], 0, v[164:165]
	s_mov_b32 m0, s73
	s_nop 0
	global_load_lds_dwordx4 v[14:15], off
	s_waitcnt vmcnt(8) lgkmcnt(0)
	s_barrier
	v_lshl_add_u64 v[12:13], s[50:51], 0, v[166:167]
	v_lshl_add_u64 v[10:11], s[50:51], 0, v[252:253]
	s_setprio 1
	v_mfma_f32_16x16x128_f8f6f4 v[94:97], v[188:195], v[204:211], v[94:97]
	v_mfma_f32_16x16x128_f8f6f4 v[82:85], v[196:203], v[204:211], v[82:85]
	v_mfma_f32_16x16x128_f8f6f4 v[74:77], v[188:195], v[212:219], v[74:77]
	v_mfma_f32_16x16x128_f8f6f4 v[66:69], v[196:203], v[212:219], v[66:69]
	v_mfma_f32_16x16x128_f8f6f4 v[58:61], v[188:195], v[220:227], v[58:61]
	v_mfma_f32_16x16x128_f8f6f4 v[50:53], v[196:203], v[220:227], v[50:53]
	v_mfma_f32_16x16x128_f8f6f4 v[42:45], v[188:195], v[244:251], v[42:45]
	v_mfma_f32_16x16x128_f8f6f4 v[34:37], v[196:203], v[244:251], v[34:37]
	v_mfma_f32_16x16x128_f8f6f4 v[102:105], v[228:235], v[204:211], v[102:105]
	v_mfma_f32_16x16x128_f8f6f4 v[86:89], v[236:243], v[204:211], v[86:89]
	v_mfma_f32_16x16x128_f8f6f4 v[78:81], v[228:235], v[212:219], v[78:81]
	v_mfma_f32_16x16x128_f8f6f4 v[70:73], v[236:243], v[212:219], v[70:73]
	v_mfma_f32_16x16x128_f8f6f4 v[62:65], v[228:235], v[220:227], v[62:65]
	v_mfma_f32_16x16x128_f8f6f4 v[54:57], v[236:243], v[220:227], v[54:57]
	v_mfma_f32_16x16x128_f8f6f4 v[46:49], v[228:235], v[244:251], v[46:49]
	v_mfma_f32_16x16x128_f8f6f4 v[38:41], v[236:243], v[244:251], v[38:41]
	s_setprio 0
	s_barrier
	ds_read_b128 v[188:191], v185
	ds_read_b128 v[192:195], v185 offset:1024
	ds_read_b128 v[196:199], v185 offset:2048
	ds_read_b128 v[200:203], v185 offset:3072
	s_mov_b32 m0, s57
	ds_read_b128 v[204:207], v177 offset:32768
	ds_read_b128 v[208:211], v177 offset:33792
	ds_read_b128 v[212:215], v177 offset:34816
	ds_read_b128 v[216:219], v177 offset:35840
	ds_read_b128 v[220:223], v177 offset:36864
	ds_read_b128 v[224:227], v177 offset:37888
	ds_read_b128 v[228:231], v177 offset:38912
	ds_read_b128 v[232:235], v177 offset:39936
	global_load_lds_dwordx4 v169, s[50:51]
	s_mov_b32 m0, s58
	s_nop 0
	global_load_lds_dwordx4 v171, s[50:51]
	ds_read_b128 v[236:239], v186
	ds_read_b128 v[240:243], v186 offset:1024
	ds_read_b128 v[244:247], v186 offset:2048
	ds_read_b128 v[248:251], v186 offset:3072
	s_waitcnt vmcnt(8) lgkmcnt(0)
	s_barrier
	s_setprio 1
	v_mfma_f32_16x16x128_f8f6f4 v[154:157], v[188:195], v[204:211], v[154:157]
	v_mfma_f32_16x16x128_f8f6f4 v[146:149], v[196:203], v[204:211], v[146:149]
	v_mfma_f32_16x16x128_f8f6f4 v[138:141], v[188:195], v[212:219], v[138:141]
	v_mfma_f32_16x16x128_f8f6f4 v[130:133], v[196:203], v[212:219], v[130:133]
	v_mfma_f32_16x16x128_f8f6f4 v[122:125], v[188:195], v[220:227], v[122:125]
	v_mfma_f32_16x16x128_f8f6f4 v[114:117], v[196:203], v[220:227], v[114:117]
	v_mfma_f32_16x16x128_f8f6f4 v[106:109], v[188:195], v[228:235], v[106:109]
	v_mfma_f32_16x16x128_f8f6f4 v[90:93], v[196:203], v[228:235], v[90:93]
	v_mfma_f32_16x16x128_f8f6f4 v[158:161], v[236:243], v[204:211], v[158:161]
	v_mfma_f32_16x16x128_f8f6f4 v[150:153], v[244:251], v[204:211], v[150:153]
	v_mfma_f32_16x16x128_f8f6f4 v[142:145], v[236:243], v[212:219], v[142:145]
	v_mfma_f32_16x16x128_f8f6f4 v[134:137], v[244:251], v[212:219], v[134:137]
	v_mfma_f32_16x16x128_f8f6f4 v[126:129], v[236:243], v[220:227], v[126:129]
	v_mfma_f32_16x16x128_f8f6f4 v[118:121], v[244:251], v[220:227], v[118:121]
	v_mfma_f32_16x16x128_f8f6f4 v[110:113], v[236:243], v[228:235], v[110:113]
	v_mfma_f32_16x16x128_f8f6f4 v[98:101], v[244:251], v[228:235], v[98:101]
	s_setprio 0
	s_barrier
	ds_read_b128 v[204:207], v177 offset:49152
	ds_read_b128 v[208:211], v177 offset:50176
	ds_read_b128 v[212:215], v177 offset:51200
	ds_read_b128 v[216:219], v177 offset:52224
	ds_read_b128 v[220:223], v177 offset:53248
	ds_read_b128 v[224:227], v177 offset:54272
	ds_read_b128 v[228:231], v177 offset:55296
	ds_read_b128 v[232:235], v177 offset:56320
	s_mov_b32 m0, s74
	v_lshl_add_u64 v[6:7], v[6:7], 0, s[18:19]
	global_load_lds_dwordx4 v[6:7], off
	v_lshl_add_u64 v[6:7], v[8:9], 0, s[18:19]
	s_mov_b32 m0, s75
	s_nop 0
	global_load_lds_dwordx4 v[6:7], off
	s_mov_b32 m0, s60
	v_lshl_add_u64 v[6:7], v[12:13], 0, s[18:19]
	global_load_lds_dwordx4 v[6:7], off
	v_lshl_add_u64 v[6:7], v[10:11], 0, s[18:19]
	s_mov_b32 m0, s61
	s_nop 0
	global_load_lds_dwordx4 v[6:7], off
	s_add_u32 s48, s48, 0x40080
	s_addc_u32 s49, s49, 0
	s_mov_b32 m0, s76
	v_lshl_add_u64 v[6:7], s[48:49], 0, v[162:163]
	global_load_lds_dwordx4 v[6:7], off
	v_lshl_add_u64 v[6:7], s[48:49], 0, v[164:165]
	s_mov_b32 m0, s77
	s_nop 0
	global_load_lds_dwordx4 v[6:7], off
	s_waitcnt vmcnt(8) lgkmcnt(0)
	s_barrier
	s_setprio 1
	v_mfma_f32_16x16x128_f8f6f4 v[94:97], v[188:195], v[204:211], v[94:97]
	v_mfma_f32_16x16x128_f8f6f4 v[82:85], v[196:203], v[204:211], v[82:85]
	v_mfma_f32_16x16x128_f8f6f4 v[74:77], v[188:195], v[212:219], v[74:77]
	v_mfma_f32_16x16x128_f8f6f4 v[66:69], v[196:203], v[212:219], v[66:69]
	v_mfma_f32_16x16x128_f8f6f4 v[58:61], v[188:195], v[220:227], v[58:61]
	v_mfma_f32_16x16x128_f8f6f4 v[50:53], v[196:203], v[220:227], v[50:53]
	v_mfma_f32_16x16x128_f8f6f4 v[42:45], v[188:195], v[228:235], v[42:45]
	v_mfma_f32_16x16x128_f8f6f4 v[34:37], v[196:203], v[228:235], v[34:37]
	v_mfma_f32_16x16x128_f8f6f4 v[102:105], v[236:243], v[204:211], v[102:105]
	v_mfma_f32_16x16x128_f8f6f4 v[86:89], v[244:251], v[204:211], v[86:89]
	v_mfma_f32_16x16x128_f8f6f4 v[78:81], v[236:243], v[212:219], v[78:81]
	v_mfma_f32_16x16x128_f8f6f4 v[70:73], v[244:251], v[212:219], v[70:73]
	v_mfma_f32_16x16x128_f8f6f4 v[62:65], v[236:243], v[220:227], v[62:65]
	v_mfma_f32_16x16x128_f8f6f4 v[54:57], v[244:251], v[220:227], v[54:57]
	v_mfma_f32_16x16x128_f8f6f4 v[46:49], v[236:243], v[228:235], v[46:49]
	v_mfma_f32_16x16x128_f8f6f4 v[38:41], v[244:251], v[228:235], v[38:41]
	s_setprio 0
	s_add_i32 s80, s80, 2
	s_add_u32 s46, s46, 0x100
	s_addc_u32 s47, s47, 0
	s_cmp_gt_u32 s80, 13
	s_barrier
	s_cbranch_scc0 .LBB0_1442
	v_mov_b32_e32 v2, v0
	s_nop 15
	s_nop 15
	s_waitcnt vmcnt(6)
	s_lshl_b32 s41, s68, 8
	v_readfirstlane_b32 s39, v2
	v_pk_fma_f32 v[10:11], v[154:155], s[30:31], v[30:31] op_sel_hi:[1,0,1]
	s_ashr_i32 s45, s39, 2
	v_min_f32_e32 v10, 0x40e00000, v10
	v_min_f32_e32 v11, 0x40e00000, v11
	s_andn2_b32 s45, s45, 63
	v_pk_mul_f32 v[12:13], v[10:11], s[34:35] op_sel_hi:[1,0]
	s_add_i32 s45, s45, s41
	v_exp_f32_e32 v12, v12
	v_exp_f32_e32 v13, v13
	v_and_or_b32 v6, v2, 15, s45
	v_lshrrev_b32_e32 v2, 1, v2
	v_and_b32_e32 v8, 24, v2
	v_pk_fma_f32 v[2:3], v[156:157], s[30:31], v[32:33] op_sel_hi:[1,0,1]
	v_pk_add_f32 v[12:13], v[12:13], 1.0 op_sel_hi:[1,0]
	v_min_f32_e32 v2, 0x40e00000, v2
	v_min_f32_e32 v3, 0x40e00000, v3
	v_pk_mul_f32 v[154:155], v[2:3], s[34:35] op_sel_hi:[1,0]
	v_rcp_f32_e32 v12, v12
	v_rcp_f32_e32 v13, v13
	v_exp_f32_e32 v154, v154
	v_exp_f32_e32 v155, v155
	v_pk_fma_f32 v[16:17], v[158:159], s[30:31], v[26:27] op_sel_hi:[1,0,1]
	v_pk_fma_f32 v[14:15], v[160:161], s[30:31], v[28:29] op_sel_hi:[1,0,1]
	v_med3_f32 v16, v16, s65, v179
	v_med3_f32 v17, v17, s65, v179
	v_pk_fma_f32 v[10:11], v[16:17], v[10:11], v[10:11]
	v_med3_f32 v14, v14, s65, v179
	v_med3_f32 v15, v15, s65, v179
	v_pk_mul_f32 v[10:11], v[10:11], v[12:13]
	v_pk_add_f32 v[12:13], v[154:155], 1.0 op_sel_hi:[1,0]
	v_pk_fma_f32 v[2:3], v[14:15], v[2:3], v[2:3]
	v_pk_fma_f32 v[14:15], v[146:147], s[30:31], v[22:23] op_sel_hi:[1,0,1]
	v_rcp_f32_e32 v12, v12
	v_rcp_f32_e32 v13, v13
	v_min_f32_e32 v14, 0x40e00000, v14
	v_min_f32_e32 v15, 0x40e00000, v15
	v_pk_mul_f32 v[146:147], v[14:15], s[34:35] op_sel_hi:[1,0]
	v_pk_mul_f32 v[2:3], v[2:3], v[12:13]
	v_exp_f32_e32 v146, v146
	v_exp_f32_e32 v147, v147
	v_pk_fma_f32 v[12:13], v[148:149], s[30:31], v[24:25] op_sel_hi:[1,0,1]
	v_pk_fma_f32 v[148:149], v[150:151], s[30:31], v[18:19] op_sel_hi:[1,0,1]
	v_min_f32_e32 v12, 0x40e00000, v12
	v_med3_f32 v148, v148, s65, v179
	v_med3_f32 v149, v149, s65, v179
	v_min_f32_e32 v13, 0x40e00000, v13
	v_pk_add_f32 v[146:147], v[146:147], 1.0 op_sel_hi:[1,0]
	v_pk_fma_f32 v[14:15], v[148:149], v[14:15], v[14:15]
	v_pk_mul_f32 v[148:149], v[12:13], s[34:35] op_sel_hi:[1,0]
	v_rcp_f32_e32 v146, v146
	v_rcp_f32_e32 v147, v147
	v_exp_f32_e32 v148, v148
	v_exp_f32_e32 v149, v149
	v_pk_fma_f32 v[16:17], v[152:153], s[30:31], v[20:21] op_sel_hi:[1,0,1]
	v_pk_mul_f32 v[14:15], v[14:15], v[146:147]
	v_med3_f32 v16, v16, s65, v179
	v_pk_add_f32 v[146:147], v[148:149], 1.0 op_sel_hi:[1,0]
	v_mov_b32_e32 v149, v167
	v_cvt_pk_fp8_f32 v149, v14, v15
	v_pk_fma_f32 v[14:15], v[138:139], s[30:31], v[30:31] op_sel_hi:[1,0,1]
	v_med3_f32 v17, v17, s65, v179
	v_mov_b32_e32 v148, v167
	v_min_f32_e32 v14, 0x40e00000, v14
	v_min_f32_e32 v15, 0x40e00000, v15
	v_cvt_pk_fp8_f32 v148, v10, v11
	v_pk_fma_f32 v[10:11], v[16:17], v[12:13], v[12:13]
	v_pk_mul_f32 v[16:17], v[14:15], s[34:35] op_sel_hi:[1,0]
	v_pk_fma_f32 v[12:13], v[140:141], s[30:31], v[32:33] op_sel_hi:[1,0,1]
	v_exp_f32_e32 v16, v16
	v_exp_f32_e32 v17, v17
	v_min_f32_e32 v12, 0x40e00000, v12
	v_min_f32_e32 v13, 0x40e00000, v13
	v_pk_fma_f32 v[140:141], v[142:143], s[30:31], v[26:27] op_sel_hi:[1,0,1]
	v_pk_add_f32 v[16:17], v[16:17], 1.0 op_sel_hi:[1,0]
	v_pk_mul_f32 v[142:143], v[12:13], s[34:35] op_sel_hi:[1,0]
	v_rcp_f32_e32 v16, v16
	v_rcp_f32_e32 v17, v17
	v_exp_f32_e32 v142, v142
	v_exp_f32_e32 v143, v143
	v_med3_f32 v140, v140, s65, v179
	v_med3_f32 v141, v141, s65, v179
	v_pk_fma_f32 v[14:15], v[140:141], v[14:15], v[14:15]
	v_pk_fma_f32 v[138:139], v[144:145], s[30:31], v[28:29] op_sel_hi:[1,0,1]
	v_pk_mul_f32 v[14:15], v[14:15], v[16:17]
	v_pk_add_f32 v[16:17], v[142:143], 1.0 op_sel_hi:[1,0]
	v_med3_f32 v138, v138, s65, v179
	v_rcp_f32_e32 v16, v16
	v_rcp_f32_e32 v17, v17
	v_med3_f32 v139, v139, s65, v179
	v_pk_fma_f32 v[130:131], v[130:131], s[30:31], v[22:23] op_sel_hi:[1,0,1]
	v_pk_fma_f32 v[12:13], v[138:139], v[12:13], v[12:13]
	v_min_f32_e32 v130, 0x40e00000, v130
	v_min_f32_e32 v131, 0x40e00000, v131
	v_pk_mul_f32 v[12:13], v[12:13], v[16:17]
	v_pk_fma_f32 v[16:17], v[132:133], s[30:31], v[24:25] op_sel_hi:[1,0,1]
	v_pk_fma_f32 v[132:133], v[136:137], s[30:31], v[20:21] op_sel_hi:[1,0,1]
	v_pk_mul_f32 v[136:137], v[130:131], s[34:35] op_sel_hi:[1,0]
	v_pk_fma_f32 v[134:135], v[134:135], s[30:31], v[18:19] op_sel_hi:[1,0,1]
	v_exp_f32_e32 v136, v136
	v_exp_f32_e32 v137, v137
	v_med3_f32 v134, v134, s65, v179
	v_med3_f32 v135, v135, s65, v179
	v_min_f32_e32 v16, 0x40e00000, v16
	v_min_f32_e32 v17, 0x40e00000, v17
	v_pk_fma_f32 v[130:131], v[134:135], v[130:131], v[130:131]
	v_pk_mul_f32 v[134:135], v[16:17], s[34:35] op_sel_hi:[1,0]
	v_pk_add_f32 v[136:137], v[136:137], 1.0 op_sel_hi:[1,0]
	v_exp_f32_e32 v134, v134
	v_exp_f32_e32 v135, v135
	v_rcp_f32_e32 v136, v136
	v_rcp_f32_e32 v137, v137
	v_med3_f32 v132, v132, s65, v179
	v_pk_add_f32 v[134:135], v[134:135], 1.0 op_sel_hi:[1,0]
	v_med3_f32 v133, v133, s65, v179
	v_pk_mul_f32 v[130:131], v[130:131], v[136:137]
	v_rcp_f32_e32 v134, v134
	v_rcp_f32_e32 v135, v135
	v_mov_b32_e32 v137, v167
	v_cvt_pk_fp8_f32 v137, v130, v131
	v_mov_b32_e32 v136, v167
	v_cvt_pk_fp8_f32 v136, v14, v15
	v_pk_fma_f32 v[14:15], v[132:133], v[16:17], v[16:17]
	v_pk_fma_f32 v[114:115], v[114:115], s[30:31], v[22:23] op_sel_hi:[1,0,1]
	v_pk_mul_f32 v[14:15], v[14:15], v[134:135]
	v_cvt_pk_fp8_f32 v136, v12, v13 op_sel:[0,0,1]
	v_cvt_pk_fp8_f32 v137, v14, v15 op_sel:[0,0,1]
	v_pk_fma_f32 v[14:15], v[122:123], s[30:31], v[30:31] op_sel_hi:[1,0,1]
	v_pk_fma_f32 v[12:13], v[124:125], s[30:31], v[32:33] op_sel_hi:[1,0,1]
	v_min_f32_e32 v14, 0x40e00000, v14
	v_min_f32_e32 v15, 0x40e00000, v15
	v_pk_mul_f32 v[16:17], v[14:15], s[34:35] op_sel_hi:[1,0]
	v_min_f32_e32 v12, 0x40e00000, v12
	v_exp_f32_e32 v16, v16
	v_exp_f32_e32 v17, v17
	v_min_f32_e32 v13, 0x40e00000, v13
	v_pk_fma_f32 v[124:125], v[126:127], s[30:31], v[26:27] op_sel_hi:[1,0,1]
	v_pk_mul_f32 v[126:127], v[12:13], s[34:35] op_sel_hi:[1,0]
	v_pk_add_f32 v[16:17], v[16:17], 1.0 op_sel_hi:[1,0]
	v_exp_f32_e32 v126, v126
	v_rcp_f32_e32 v16, v16
	v_rcp_f32_e32 v17, v17
	v_exp_f32_e32 v127, v127
	v_med3_f32 v124, v124, s65, v179
	v_med3_f32 v125, v125, s65, v179
	v_pk_fma_f32 v[14:15], v[124:125], v[14:15], v[14:15]
	v_pk_fma_f32 v[122:123], v[128:129], s[30:31], v[28:29] op_sel_hi:[1,0,1]
	v_pk_mul_f32 v[14:15], v[14:15], v[16:17]
	v_pk_add_f32 v[16:17], v[126:127], 1.0 op_sel_hi:[1,0]
	v_med3_f32 v122, v122, s65, v179
	v_rcp_f32_e32 v16, v16
	v_rcp_f32_e32 v17, v17
	v_med3_f32 v123, v123, s65, v179
	v_pk_fma_f32 v[12:13], v[122:123], v[12:13], v[12:13]
	v_min_f32_e32 v114, 0x40e00000, v114
	v_min_f32_e32 v115, 0x40e00000, v115
	v_pk_mul_f32 v[12:13], v[12:13], v[16:17]
	v_pk_fma_f32 v[16:17], v[116:117], s[30:31], v[24:25] op_sel_hi:[1,0,1]
	v_pk_fma_f32 v[116:117], v[120:121], s[30:31], v[20:21] op_sel_hi:[1,0,1]
	v_pk_mul_f32 v[120:121], v[114:115], s[34:35] op_sel_hi:[1,0]
	v_pk_fma_f32 v[118:119], v[118:119], s[30:31], v[18:19] op_sel_hi:[1,0,1]
	v_exp_f32_e32 v120, v120
	v_exp_f32_e32 v121, v121
	v_med3_f32 v118, v118, s65, v179
	v_med3_f32 v119, v119, s65, v179
	v_min_f32_e32 v16, 0x40e00000, v16
	v_min_f32_e32 v17, 0x40e00000, v17
	v_rcp_f32_e32 v146, v146
	v_rcp_f32_e32 v147, v147
	v_pk_add_f32 v[120:121], v[120:121], 1.0 op_sel_hi:[1,0]
	v_pk_fma_f32 v[114:115], v[118:119], v[114:115], v[114:115]
	v_pk_mul_f32 v[118:119], v[16:17], s[34:35] op_sel_hi:[1,0]
	v_rcp_f32_e32 v120, v120
	v_rcp_f32_e32 v121, v121
	v_exp_f32_e32 v118, v118
	v_exp_f32_e32 v119, v119
	s_lshr_b32 s39, s39, 1
	v_pk_mul_f32 v[10:11], v[10:11], v[146:147]
	s_lshl_b32 s41, s44, 7
	s_and_b32 s39, s39, 0x60
	v_cvt_pk_fp8_f32 v149, v10, v11 op_sel:[0,0,1]
	v_or_b32_e32 v10, 16, v6
	v_pk_mul_f32 v[114:115], v[114:115], v[120:121]
	v_pk_add_f32 v[118:119], v[118:119], 1.0 op_sel_hi:[1,0]
	v_mov_b32_e32 v120, v167
	s_or_b32 s41, s39, s41
	v_ashrrev_i32_e32 v11, 31, v10
	v_rcp_f32_e32 v118, v118
	v_rcp_f32_e32 v119, v119
	v_cvt_pk_fp8_f32 v120, v14, v15
	v_mov_b32_e32 v121, v167
	v_or_b32_e32 v4, s41, v8
	v_lshlrev_b64 v[10:11], 11, v[10:11]
	v_cvt_pk_fp8_f32 v121, v114, v115
	v_ashrrev_i32_e32 v5, 31, v4
	v_lshl_add_u64 v[10:11], s[16:17], 0, v[10:11]
	v_med3_f32 v116, v116, s65, v179
	v_med3_f32 v117, v117, s65, v179
	v_lshl_add_u64 v[10:11], v[10:11], 0, v[4:5]
	v_pk_fma_f32 v[14:15], v[116:117], v[16:17], v[16:17]
	global_store_dwordx2 v[10:11], v[136:137], off
	v_or_b32_e32 v10, 32, v6
	v_pk_mul_f32 v[14:15], v[14:15], v[118:119]
	v_cvt_pk_fp8_f32 v120, v12, v13 op_sel:[0,0,1]
	v_pk_fma_f32 v[12:13], v[106:107], s[30:31], v[30:31] op_sel_hi:[1,0,1]
	v_ashrrev_i32_e32 v11, 31, v10
	v_cvt_pk_fp8_f32 v121, v14, v15 op_sel:[0,0,1]
	v_min_f32_e32 v12, 0x40e00000, v12
	v_min_f32_e32 v13, 0x40e00000, v13
	v_lshlrev_b64 v[10:11], 11, v[10:11]
	v_pk_mul_f32 v[14:15], v[12:13], s[34:35] op_sel_hi:[1,0]
	v_lshl_add_u64 v[10:11], s[16:17], 0, v[10:11]
	v_exp_f32_e32 v14, v14
	v_exp_f32_e32 v15, v15
	v_lshl_add_u64 v[10:11], v[10:11], 0, v[4:5]
	global_store_dwordx2 v[10:11], v[120:121], off
	v_pk_fma_f32 v[10:11], v[108:109], s[30:31], v[32:33] op_sel_hi:[1,0,1]
	v_pk_add_f32 v[14:15], v[14:15], 1.0 op_sel_hi:[1,0]
	v_min_f32_e32 v10, 0x40e00000, v10
	v_min_f32_e32 v11, 0x40e00000, v11
	v_pk_mul_f32 v[108:109], v[10:11], s[34:35] op_sel_hi:[1,0]
	v_rcp_f32_e32 v14, v14
	v_rcp_f32_e32 v15, v15
	v_exp_f32_e32 v108, v108
	v_exp_f32_e32 v109, v109
	v_pk_fma_f32 v[106:107], v[110:111], s[30:31], v[26:27] op_sel_hi:[1,0,1]
	v_pk_fma_f32 v[16:17], v[112:113], s[30:31], v[28:29] op_sel_hi:[1,0,1]
	v_med3_f32 v106, v106, s65, v179
	v_med3_f32 v107, v107, s65, v179
	v_pk_fma_f32 v[12:13], v[106:107], v[12:13], v[12:13]
	v_med3_f32 v16, v16, s65, v179
	v_pk_mul_f32 v[12:13], v[12:13], v[14:15]
	v_pk_add_f32 v[14:15], v[108:109], 1.0 op_sel_hi:[1,0]
	v_med3_f32 v17, v17, s65, v179
	v_rcp_f32_e32 v14, v14
	v_rcp_f32_e32 v15, v15
	v_pk_fma_f32 v[10:11], v[16:17], v[10:11], v[10:11]
	v_pk_fma_f32 v[16:17], v[90:91], s[30:31], v[22:23] op_sel_hi:[1,0,1]
	v_pk_fma_f32 v[98:99], v[98:99], s[30:31], v[18:19] op_sel_hi:[1,0,1]
	v_min_f32_e32 v16, 0x40e00000, v16
	v_min_f32_e32 v17, 0x40e00000, v17
	v_pk_mul_f32 v[10:11], v[10:11], v[14:15]
	v_pk_fma_f32 v[14:15], v[92:93], s[30:31], v[24:25] op_sel_hi:[1,0,1]
	v_pk_mul_f32 v[92:93], v[16:17], s[34:35] op_sel_hi:[1,0]
	v_med3_f32 v98, v98, s65, v179
	v_exp_f32_e32 v92, v92
	v_exp_f32_e32 v93, v93
	v_med3_f32 v99, v99, s65, v179
	v_min_f32_e32 v14, 0x40e00000, v14
	v_min_f32_e32 v15, 0x40e00000, v15
	v_pk_add_f32 v[92:93], v[92:93], 1.0 op_sel_hi:[1,0]
	v_pk_fma_f32 v[16:17], v[98:99], v[16:17], v[16:17]
	v_pk_mul_f32 v[98:99], v[14:15], s[34:35] op_sel_hi:[1,0]
	v_rcp_f32_e32 v92, v92
	v_rcp_f32_e32 v93, v93
	v_exp_f32_e32 v98, v98
	v_exp_f32_e32 v99, v99
	v_ashrrev_i32_e32 v7, 31, v6
	v_pk_mul_f32 v[16:17], v[16:17], v[92:93]
	v_cvt_pk_fp8_f32 v148, v2, v3 op_sel:[0,0,1]
	v_pk_add_f32 v[92:93], v[98:99], 1.0 op_sel_hi:[1,0]
	v_lshlrev_b64 v[2:3], 11, v[6:7]
	v_or_b32_e32 v6, 48, v6
	v_rcp_f32_e32 v92, v92
	v_rcp_f32_e32 v93, v93
	v_mov_b32_e32 v98, v167
	v_mov_b32_e32 v99, v167
	v_ashrrev_i32_e32 v7, 31, v6
	v_pk_fma_f32 v[90:91], v[100:101], s[30:31], v[20:21] op_sel_hi:[1,0,1]
	v_cvt_pk_fp8_f32 v98, v12, v13
	v_cvt_pk_fp8_f32 v99, v16, v17
	v_med3_f32 v90, v90, s65, v179
	v_med3_f32 v91, v91, s65, v179
	v_lshlrev_b64 v[6:7], 11, v[6:7]
	v_lshl_add_u64 v[2:3], s[16:17], 0, v[2:3]
	v_pk_fma_f32 v[12:13], v[90:91], v[14:15], v[14:15]
	v_lshl_add_u64 v[6:7], s[16:17], 0, v[6:7]
	v_lshl_add_u64 v[2:3], v[2:3], 0, v[4:5]
	v_pk_mul_f32 v[12:13], v[12:13], v[92:93]
	v_lshl_add_u64 v[4:5], v[6:7], 0, v[4:5]
	v_pk_fma_f32 v[6:7], v[94:95], s[30:31], v[30:31] op_sel_hi:[1,0,1]
	v_cvt_pk_fp8_f32 v98, v10, v11 op_sel:[0,0,1]
	v_cvt_pk_fp8_f32 v99, v12, v13 op_sel:[0,0,1]
	v_min_f32_e32 v6, 0x40e00000, v6
	v_min_f32_e32 v7, 0x40e00000, v7
	v_pk_mul_f32 v[10:11], v[6:7], s[34:35] op_sel_hi:[1,0]
	global_store_dwordx2 v[4:5], v[98:99], off
	v_exp_f32_e32 v10, v10
	v_exp_f32_e32 v11, v11
	v_pk_fma_f32 v[4:5], v[96:97], s[30:31], v[32:33] op_sel_hi:[1,0,1]
	v_pk_fma_f32 v[14:15], v[102:103], s[30:31], v[26:27] op_sel_hi:[1,0,1]
	v_min_f32_e32 v4, 0x40e00000, v4
	v_min_f32_e32 v5, 0x40e00000, v5
	v_pk_add_f32 v[10:11], v[10:11], 1.0 op_sel_hi:[1,0]
	v_pk_mul_f32 v[16:17], v[4:5], s[34:35] op_sel_hi:[1,0]
	v_rcp_f32_e32 v10, v10
	v_rcp_f32_e32 v11, v11
	v_exp_f32_e32 v16, v16
	v_exp_f32_e32 v17, v17
	v_pk_fma_f32 v[12:13], v[104:105], s[30:31], v[28:29] op_sel_hi:[1,0,1]
	v_med3_f32 v14, v14, s65, v179
	v_med3_f32 v15, v15, s65, v179
	v_pk_fma_f32 v[6:7], v[14:15], v[6:7], v[6:7]
	v_med3_f32 v12, v12, s65, v179
	v_med3_f32 v13, v13, s65, v179
	v_pk_mul_f32 v[6:7], v[6:7], v[10:11]
	v_pk_add_f32 v[10:11], v[16:17], 1.0 op_sel_hi:[1,0]
	v_pk_fma_f32 v[4:5], v[12:13], v[4:5], v[4:5]
	v_pk_fma_f32 v[12:13], v[82:83], s[30:31], v[22:23] op_sel_hi:[1,0,1]
	v_rcp_f32_e32 v10, v10
	v_rcp_f32_e32 v11, v11
	v_min_f32_e32 v12, 0x40e00000, v12
	v_min_f32_e32 v13, 0x40e00000, v13
	v_pk_mul_f32 v[16:17], v[12:13], s[34:35] op_sel_hi:[1,0]
	v_pk_mul_f32 v[4:5], v[4:5], v[10:11]
	v_exp_f32_e32 v16, v16
	v_exp_f32_e32 v17, v17
	v_pk_fma_f32 v[10:11], v[84:85], s[30:31], v[24:25] op_sel_hi:[1,0,1]
	v_pk_fma_f32 v[82:83], v[86:87], s[30:31], v[18:19] op_sel_hi:[1,0,1]
	v_min_f32_e32 v10, 0x40e00000, v10
	v_med3_f32 v82, v82, s65, v179
	v_med3_f32 v83, v83, s65, v179
	v_min_f32_e32 v11, 0x40e00000, v11
	v_pk_add_f32 v[16:17], v[16:17], 1.0 op_sel_hi:[1,0]
	v_pk_fma_f32 v[12:13], v[82:83], v[12:13], v[12:13]
	v_pk_mul_f32 v[82:83], v[10:11], s[34:35] op_sel_hi:[1,0]
	v_rcp_f32_e32 v16, v16
	v_rcp_f32_e32 v17, v17
	v_exp_f32_e32 v82, v82
	v_exp_f32_e32 v83, v83
	v_pk_fma_f32 v[14:15], v[88:89], s[30:31], v[20:21] op_sel_hi:[1,0,1]
	v_pk_mul_f32 v[12:13], v[12:13], v[16:17]
	v_med3_f32 v14, v14, s65, v179
	v_pk_add_f32 v[16:17], v[82:83], 1.0 op_sel_hi:[1,0]
	v_mov_b32_e32 v83, v167
	v_rcp_f32_e32 v16, v16
	v_rcp_f32_e32 v17, v17
	v_mov_b32_e32 v82, v167
	v_cvt_pk_fp8_f32 v83, v12, v13
	v_med3_f32 v15, v15, s65, v179
	v_cvt_pk_fp8_f32 v82, v6, v7
	v_pk_fma_f32 v[6:7], v[14:15], v[10:11], v[10:11]
	s_mov_b32 s41, 0x40000
	v_pk_mul_f32 v[6:7], v[6:7], v[16:17]
	v_cvt_pk_fp8_f32 v82, v4, v5 op_sel:[0,0,1]
	v_cvt_pk_fp8_f32 v83, v6, v7 op_sel:[0,0,1]
	v_pk_fma_f32 v[6:7], v[74:75], s[30:31], v[30:31] op_sel_hi:[1,0,1]
	v_add_co_u32_e32 v4, vcc, s41, v2
	v_min_f32_e32 v6, 0x40e00000, v6
	v_min_f32_e32 v7, 0x40e00000, v7
	v_pk_mul_f32 v[10:11], v[6:7], s[34:35] op_sel_hi:[1,0]
	v_addc_co_u32_e32 v5, vcc, 0, v3, vcc
	v_exp_f32_e32 v10, v10
	v_exp_f32_e32 v11, v11
	global_store_dwordx2 v[4:5], v[82:83], off
	v_pk_fma_f32 v[4:5], v[76:77], s[30:31], v[32:33] op_sel_hi:[1,0,1]
	v_pk_fma_f32 v[14:15], v[78:79], s[30:31], v[26:27] op_sel_hi:[1,0,1]
	v_min_f32_e32 v4, 0x40e00000, v4
	v_min_f32_e32 v5, 0x40e00000, v5
	v_pk_add_f32 v[10:11], v[10:11], 1.0 op_sel_hi:[1,0]
	v_pk_mul_f32 v[16:17], v[4:5], s[34:35] op_sel_hi:[1,0]
	v_rcp_f32_e32 v10, v10
	v_rcp_f32_e32 v11, v11
	v_exp_f32_e32 v16, v16
	v_exp_f32_e32 v17, v17
	v_pk_fma_f32 v[12:13], v[80:81], s[30:31], v[28:29] op_sel_hi:[1,0,1]
	v_med3_f32 v14, v14, s65, v179
	v_med3_f32 v15, v15, s65, v179
	v_pk_fma_f32 v[6:7], v[14:15], v[6:7], v[6:7]
	v_med3_f32 v12, v12, s65, v179
	v_med3_f32 v13, v13, s65, v179
	v_pk_mul_f32 v[6:7], v[6:7], v[10:11]
	v_pk_add_f32 v[10:11], v[16:17], 1.0 op_sel_hi:[1,0]
	v_pk_fma_f32 v[4:5], v[12:13], v[4:5], v[4:5]
	v_pk_fma_f32 v[12:13], v[66:67], s[30:31], v[22:23] op_sel_hi:[1,0,1]
	v_rcp_f32_e32 v10, v10
	v_rcp_f32_e32 v11, v11
	v_min_f32_e32 v12, 0x40e00000, v12
	v_min_f32_e32 v13, 0x40e00000, v13
	v_pk_mul_f32 v[16:17], v[12:13], s[34:35] op_sel_hi:[1,0]
	v_pk_mul_f32 v[4:5], v[4:5], v[10:11]
	v_exp_f32_e32 v16, v16
	v_exp_f32_e32 v17, v17
	v_pk_fma_f32 v[10:11], v[68:69], s[30:31], v[24:25] op_sel_hi:[1,0,1]
	v_pk_fma_f32 v[66:67], v[70:71], s[30:31], v[18:19] op_sel_hi:[1,0,1]
	v_min_f32_e32 v10, 0x40e00000, v10
	v_med3_f32 v66, v66, s65, v179
	v_med3_f32 v67, v67, s65, v179
	v_min_f32_e32 v11, 0x40e00000, v11
	v_pk_add_f32 v[16:17], v[16:17], 1.0 op_sel_hi:[1,0]
	v_pk_fma_f32 v[12:13], v[66:67], v[12:13], v[12:13]
	v_pk_mul_f32 v[66:67], v[10:11], s[34:35] op_sel_hi:[1,0]
	v_rcp_f32_e32 v16, v16
	v_rcp_f32_e32 v17, v17
	v_exp_f32_e32 v66, v66
	v_exp_f32_e32 v67, v67
	v_pk_fma_f32 v[14:15], v[72:73], s[30:31], v[20:21] op_sel_hi:[1,0,1]
	v_pk_mul_f32 v[12:13], v[12:13], v[16:17]
	v_med3_f32 v14, v14, s65, v179
	v_pk_add_f32 v[16:17], v[66:67], 1.0 op_sel_hi:[1,0]
	v_mov_b32_e32 v67, v167
	v_rcp_f32_e32 v16, v16
	v_rcp_f32_e32 v17, v17
	v_mov_b32_e32 v66, v167
	v_cvt_pk_fp8_f32 v67, v12, v13
	v_med3_f32 v15, v15, s65, v179
	v_cvt_pk_fp8_f32 v66, v6, v7
	v_pk_fma_f32 v[6:7], v[14:15], v[10:11], v[10:11]
	s_mov_b32 s41, 0x48000
	v_pk_mul_f32 v[6:7], v[6:7], v[16:17]
	v_cvt_pk_fp8_f32 v66, v4, v5 op_sel:[0,0,1]
	v_cvt_pk_fp8_f32 v67, v6, v7 op_sel:[0,0,1]
	v_pk_fma_f32 v[6:7], v[58:59], s[30:31], v[30:31] op_sel_hi:[1,0,1]
	v_add_co_u32_e32 v4, vcc, s41, v2
	v_min_f32_e32 v6, 0x40e00000, v6
	v_min_f32_e32 v7, 0x40e00000, v7
	v_pk_mul_f32 v[10:11], v[6:7], s[34:35] op_sel_hi:[1,0]
	v_addc_co_u32_e32 v5, vcc, 0, v3, vcc
	v_exp_f32_e32 v10, v10
	v_exp_f32_e32 v11, v11
	global_store_dwordx2 v[4:5], v[66:67], off
	v_pk_fma_f32 v[4:5], v[60:61], s[30:31], v[32:33] op_sel_hi:[1,0,1]
	v_pk_fma_f32 v[14:15], v[62:63], s[30:31], v[26:27] op_sel_hi:[1,0,1]
	v_min_f32_e32 v4, 0x40e00000, v4
	v_min_f32_e32 v5, 0x40e00000, v5
	v_pk_add_f32 v[10:11], v[10:11], 1.0 op_sel_hi:[1,0]
	v_pk_mul_f32 v[16:17], v[4:5], s[34:35] op_sel_hi:[1,0]
	v_rcp_f32_e32 v10, v10
	v_rcp_f32_e32 v11, v11
	v_exp_f32_e32 v16, v16
	v_exp_f32_e32 v17, v17
	v_pk_fma_f32 v[12:13], v[64:65], s[30:31], v[28:29] op_sel_hi:[1,0,1]
	v_med3_f32 v14, v14, s65, v179
	v_med3_f32 v15, v15, s65, v179
	v_pk_fma_f32 v[6:7], v[14:15], v[6:7], v[6:7]
	v_med3_f32 v12, v12, s65, v179
	v_med3_f32 v13, v13, s65, v179
	v_pk_mul_f32 v[6:7], v[6:7], v[10:11]
	v_pk_add_f32 v[10:11], v[16:17], 1.0 op_sel_hi:[1,0]
	v_pk_fma_f32 v[4:5], v[12:13], v[4:5], v[4:5]
	v_pk_fma_f32 v[12:13], v[50:51], s[30:31], v[22:23] op_sel_hi:[1,0,1]
	v_rcp_f32_e32 v10, v10
	v_rcp_f32_e32 v11, v11
	v_min_f32_e32 v12, 0x40e00000, v12
	v_min_f32_e32 v13, 0x40e00000, v13
	v_pk_mul_f32 v[16:17], v[12:13], s[34:35] op_sel_hi:[1,0]
	v_pk_mul_f32 v[4:5], v[4:5], v[10:11]
	v_exp_f32_e32 v16, v16
	v_exp_f32_e32 v17, v17
	v_pk_fma_f32 v[10:11], v[52:53], s[30:31], v[24:25] op_sel_hi:[1,0,1]
	v_pk_fma_f32 v[50:51], v[54:55], s[30:31], v[18:19] op_sel_hi:[1,0,1]
	v_min_f32_e32 v10, 0x40e00000, v10
	v_med3_f32 v50, v50, s65, v179
	v_med3_f32 v51, v51, s65, v179
	v_min_f32_e32 v11, 0x40e00000, v11
	v_pk_add_f32 v[16:17], v[16:17], 1.0 op_sel_hi:[1,0]
	v_pk_fma_f32 v[12:13], v[50:51], v[12:13], v[12:13]
	v_pk_mul_f32 v[50:51], v[10:11], s[34:35] op_sel_hi:[1,0]
	v_rcp_f32_e32 v16, v16
	v_rcp_f32_e32 v17, v17
	v_exp_f32_e32 v50, v50
	v_exp_f32_e32 v51, v51
	v_pk_fma_f32 v[14:15], v[56:57], s[30:31], v[20:21] op_sel_hi:[1,0,1]
	v_pk_mul_f32 v[12:13], v[12:13], v[16:17]
	v_med3_f32 v14, v14, s65, v179
	v_pk_add_f32 v[16:17], v[50:51], 1.0 op_sel_hi:[1,0]
	v_mov_b32_e32 v51, v167
	v_rcp_f32_e32 v16, v16
	v_rcp_f32_e32 v17, v17
	v_mov_b32_e32 v50, v167
	v_cvt_pk_fp8_f32 v51, v12, v13
	v_med3_f32 v15, v15, s65, v179
	v_cvt_pk_fp8_f32 v50, v6, v7
	v_pk_fma_f32 v[6:7], v[14:15], v[10:11], v[10:11]
	s_mov_b32 s41, 0x50000
	v_pk_mul_f32 v[6:7], v[6:7], v[16:17]
	v_cvt_pk_fp8_f32 v50, v4, v5 op_sel:[0,0,1]
	v_cvt_pk_fp8_f32 v51, v6, v7 op_sel:[0,0,1]
	v_pk_fma_f32 v[6:7], v[42:43], s[30:31], v[30:31] op_sel_hi:[1,0,1]
	v_add_co_u32_e32 v4, vcc, s41, v2
	v_min_f32_e32 v6, 0x40e00000, v6
	v_min_f32_e32 v7, 0x40e00000, v7
	v_pk_mul_f32 v[10:11], v[6:7], s[34:35] op_sel_hi:[1,0]
	v_addc_co_u32_e32 v5, vcc, 0, v3, vcc
	v_exp_f32_e32 v10, v10
	v_exp_f32_e32 v11, v11
	global_store_dwordx2 v[4:5], v[50:51], off
	v_pk_fma_f32 v[4:5], v[44:45], s[30:31], v[32:33] op_sel_hi:[1,0,1]
	v_pk_fma_f32 v[14:15], v[46:47], s[30:31], v[26:27] op_sel_hi:[1,0,1]
	v_min_f32_e32 v4, 0x40e00000, v4
	v_min_f32_e32 v5, 0x40e00000, v5
	v_pk_add_f32 v[10:11], v[10:11], 1.0 op_sel_hi:[1,0]
	v_pk_mul_f32 v[16:17], v[4:5], s[34:35] op_sel_hi:[1,0]
	v_rcp_f32_e32 v10, v10
	v_rcp_f32_e32 v11, v11
	v_exp_f32_e32 v16, v16
	v_exp_f32_e32 v17, v17
	v_pk_fma_f32 v[12:13], v[48:49], s[30:31], v[28:29] op_sel_hi:[1,0,1]
	v_med3_f32 v14, v14, s65, v179
	v_med3_f32 v15, v15, s65, v179
	v_pk_fma_f32 v[6:7], v[14:15], v[6:7], v[6:7]
	v_med3_f32 v12, v12, s65, v179
	v_med3_f32 v13, v13, s65, v179
	v_pk_mul_f32 v[6:7], v[6:7], v[10:11]
	v_pk_add_f32 v[10:11], v[16:17], 1.0 op_sel_hi:[1,0]
	v_pk_fma_f32 v[4:5], v[12:13], v[4:5], v[4:5]
	v_pk_fma_f32 v[12:13], v[34:35], s[30:31], v[22:23] op_sel_hi:[1,0,1]
	v_rcp_f32_e32 v10, v10
	v_rcp_f32_e32 v11, v11
	v_min_f32_e32 v12, 0x40e00000, v12
	v_min_f32_e32 v13, 0x40e00000, v13
	v_pk_mul_f32 v[16:17], v[12:13], s[34:35] op_sel_hi:[1,0]
	v_pk_mul_f32 v[4:5], v[4:5], v[10:11]
	v_exp_f32_e32 v16, v16
	v_exp_f32_e32 v17, v17
	v_pk_fma_f32 v[10:11], v[36:37], s[30:31], v[24:25] op_sel_hi:[1,0,1]
	v_pk_fma_f32 v[18:19], v[38:39], s[30:31], v[18:19] op_sel_hi:[1,0,1]
	v_min_f32_e32 v10, 0x40e00000, v10
	v_med3_f32 v18, v18, s65, v179
	v_med3_f32 v19, v19, s65, v179
	v_min_f32_e32 v11, 0x40e00000, v11
	v_pk_add_f32 v[16:17], v[16:17], 1.0 op_sel_hi:[1,0]
	v_pk_fma_f32 v[12:13], v[18:19], v[12:13], v[12:13]
	v_pk_mul_f32 v[18:19], v[10:11], s[34:35] op_sel_hi:[1,0]
	v_rcp_f32_e32 v16, v16
	v_rcp_f32_e32 v17, v17
	v_exp_f32_e32 v18, v18
	v_exp_f32_e32 v19, v19
	v_pk_fma_f32 v[14:15], v[40:41], s[30:31], v[20:21] op_sel_hi:[1,0,1]
	v_pk_mul_f32 v[12:13], v[12:13], v[16:17]
	v_med3_f32 v14, v14, s65, v179
	v_pk_add_f32 v[16:17], v[18:19], 1.0 op_sel_hi:[1,0]
	v_mov_b32_e32 v18, v167
	v_rcp_f32_e32 v16, v16
	v_rcp_f32_e32 v17, v17
	v_mov_b32_e32 v19, v167
	v_cvt_pk_fp8_f32 v18, v6, v7
	v_cvt_pk_fp8_f32 v19, v12, v13
	v_med3_f32 v15, v15, s65, v179
	v_pk_fma_f32 v[6:7], v[14:15], v[10:11], v[10:11]
	v_cvt_pk_fp8_f32 v18, v4, v5 op_sel:[0,0,1]
	v_pk_mul_f32 v[6:7], v[6:7], v[16:17]
	global_store_dwordx2 v[2:3], v[148:149], off
	v_cvt_pk_fp8_f32 v19, v6, v7 op_sel:[0,0,1]
	v_add_co_u32_e32 v2, vcc, 0x58000, v2
	s_mov_b64 s[44:45], -1
	s_nop 0
	v_addc_co_u32_e32 v3, vcc, 0, v3, vcc
	s_and_b64 vcc, s[42:43], exec
	global_store_dwordx2 v[2:3], v[18:19], off
	s_cbranch_vccz .LBB0_1434
	s_ashr_i32 s41, s40, 31
	s_lshl_b64 s[42:43], s[40:41], 14
	s_add_u32 s41, s88, s42
	s_addc_u32 s44, s89, s43
	s_lshl_b32 s42, s38, 7
	s_ashr_i32 s43, s42, 31
	s_lshl_b64 s[42:43], s[42:43], 2
	s_add_u32 s41, s41, s42
	s_addc_u32 s43, s44, s43
	s_lshl_b32 s39, s39, 2
	s_add_u32 s42, s41, s39
	s_addc_u32 s43, s43, 0
	v_lshlrev_b32_e32 v166, 2, v8
	v_lshl_add_u64 v[2:3], s[42:43], 0, v[166:167]
	v_lshl_add_u64 v[4:5], v[2:3], 0, 16
	s_mov_b64 s[44:45], 0
	global_load_dwordx4 v[30:33], v[2:3], off
	global_load_dwordx4 v[22:25], v[4:5], off
	v_lshl_add_u64 v[4:5], v[2:3], 0, s[12:13]
	global_load_dwordx4 v[26:29], v[4:5], off
	v_lshl_add_u64 v[2:3], v[2:3], 0, s[14:15]
	global_load_dwordx4 v[18:21], v[2:3], off
	s_branch .LBB0_1434

.LBB0_1546:
	s_ashr_i32 s31, s30, 31
	s_lshl_b64 s[34:35], s[30:31], 19
	s_add_u32 s34, s50, s34
	s_addc_u32 s35, s51, s35
	s_and_b64 s[36:37], s[42:43], exec
	s_cselect_b32 s27, s35, s45
	s_cselect_b32 s31, s34, s44
	s_add_u32 s39, s52, s28
	ds_read_b128 v[2:5], v183
	ds_read_b128 v[6:9], v183 offset:1024
	ds_read_b128 v[10:13], v183 offset:2048
	ds_read_b128 v[14:17], v183 offset:3072
	s_addc_u32 s48, s53, s29
	s_ashr_i32 s25, s24, 31
	s_lshl_b64 s[36:37], s[24:25], 19
	s_add_u32 s36, s39, s36
	s_addc_u32 s37, s48, s37
	s_and_b64 s[48:49], s[42:43], exec
	s_cselect_b32 s25, s37, s47
	s_cselect_b32 s39, s36, s46
	s_add_u32 s48, s44, 0x40080
	s_addc_u32 s49, s45, 0
	s_add_i32 s68, s54, 0xc000
	v_lshl_add_u64 v[66:67], s[48:49], 0, v[162:163]
	s_mov_b32 m0, s68
	s_add_i32 s69, s54, 0xe000
	ds_read_b128 v[34:37], v184
	ds_read_b128 v[38:41], v184 offset:1024
	ds_read_b128 v[42:45], v184 offset:2048
	ds_read_b128 v[46:49], v184 offset:3072
	ds_read_b128 v[50:53], v184 offset:4096
	ds_read_b128 v[54:57], v184 offset:5120
	ds_read_b128 v[58:61], v184 offset:6144
	ds_read_b128 v[62:65], v184 offset:7168
	global_load_lds_dwordx4 v[66:67], off
	v_lshl_add_u64 v[66:67], s[48:49], 0, v[166:167]
	s_mov_b32 m0, s69
	s_nop 0
	global_load_lds_dwordx4 v[66:67], off
	s_waitcnt lgkmcnt(8)
	s_barrier
	s_waitcnt lgkmcnt(0)
	s_setprio 1
	s_waitcnt lgkmcnt(0)
	v_mfma_f32_16x16x128_f8f6f4 v[150:153], v[2:9], v[34:41], 0
	v_mfma_f32_16x16x128_f8f6f4 v[146:149], v[10:17], v[34:41], 0
	v_mfma_f32_16x16x128_f8f6f4 v[134:137], v[2:9], v[42:49], 0
	v_mfma_f32_16x16x128_f8f6f4 v[130:133], v[10:17], v[42:49], 0
	v_mfma_f32_16x16x128_f8f6f4 v[118:121], v[2:9], v[50:57], 0
	v_mfma_f32_16x16x128_f8f6f4 v[114:117], v[10:17], v[50:57], 0
	v_mfma_f32_16x16x128_f8f6f4 v[86:89], v[2:9], v[58:65], 0
	v_mfma_f32_16x16x128_f8f6f4 v[82:85], v[10:17], v[58:65], 0
	s_setprio 0
	s_barrier
	v_lshl_add_u64 v[178:179], s[46:47], 0, v[164:165]
	s_add_i32 s70, s64, s41
	v_lshl_add_u64 v[66:67], v[178:179], 0, s[14:15]
	s_mov_b32 m0, s70
	v_lshl_add_u64 v[180:181], s[46:47], 0, v[168:169]
	s_add_i32 s71, s70, 0x2000
	ds_read_b128 v[186:189], v185
	ds_read_b128 v[190:193], v185 offset:1024
	ds_read_b128 v[194:197], v185 offset:2048
	ds_read_b128 v[198:201], v185 offset:3072
	global_load_lds_dwordx4 v[66:67], off
	v_lshl_add_u64 v[66:67], v[180:181], 0, s[14:15]
	s_mov_b32 m0, s71
	s_nop 0
	global_load_lds_dwordx4 v[66:67], off
	s_barrier
	s_waitcnt lgkmcnt(0)
	s_setprio 1
	s_waitcnt lgkmcnt(0)
	v_mfma_f32_16x16x128_f8f6f4 v[158:161], v[186:193], v[34:41], 0
	v_mfma_f32_16x16x128_f8f6f4 v[154:157], v[194:201], v[34:41], 0
	v_mfma_f32_16x16x128_f8f6f4 v[142:145], v[186:193], v[42:49], 0
	v_mfma_f32_16x16x128_f8f6f4 v[138:141], v[194:201], v[42:49], 0
	v_mfma_f32_16x16x128_f8f6f4 v[126:129], v[186:193], v[50:57], 0
	v_mfma_f32_16x16x128_f8f6f4 v[122:125], v[194:201], v[50:57], 0
	v_mfma_f32_16x16x128_f8f6f4 v[94:97], v[186:193], v[58:65], 0
	v_mfma_f32_16x16x128_f8f6f4 v[90:93], v[194:201], v[58:65], 0
	s_setprio 0
	v_lshl_add_u64 v[174:175], s[44:45], 0, v[162:163]
	s_mov_b32 m0, s54
	v_lshl_add_u64 v[42:43], v[174:175], 0, s[14:15]
	v_lshl_add_u64 v[176:177], s[44:45], 0, v[166:167]
	s_barrier
	ds_read_b128 v[34:37], v184 offset:16384
	ds_read_b128 v[38:41], v184 offset:17408
	ds_read_b128 v[202:205], v184 offset:18432
	ds_read_b128 v[206:209], v184 offset:19456
	ds_read_b128 v[210:213], v184 offset:20480
	ds_read_b128 v[214:217], v184 offset:21504
	ds_read_b128 v[218:221], v184 offset:22528
	ds_read_b128 v[222:225], v184 offset:23552
	global_load_lds_dwordx4 v[42:43], off
	v_lshl_add_u64 v[42:43], v[176:177], 0, s[14:15]
	s_mov_b32 m0, s55
	s_nop 0
	global_load_lds_dwordx4 v[42:43], off
	s_barrier
	s_waitcnt lgkmcnt(0)
	s_setprio 1
	s_waitcnt lgkmcnt(0)
	v_mfma_f32_16x16x128_f8f6f4 v[110:113], v[2:9], v[34:41], 0
	v_mfma_f32_16x16x128_f8f6f4 v[102:105], v[10:17], v[34:41], 0
	v_mfma_f32_16x16x128_f8f6f4 v[78:81], v[2:9], v[202:209], 0
	v_mfma_f32_16x16x128_f8f6f4 v[70:73], v[10:17], v[202:209], 0
	v_mfma_f32_16x16x128_f8f6f4 v[62:65], v[2:9], v[210:217], 0
	v_mfma_f32_16x16x128_f8f6f4 v[54:57], v[10:17], v[210:217], 0
	v_mfma_f32_16x16x128_f8f6f4 v[46:49], v[2:9], v[218:225], 0
	v_mfma_f32_16x16x128_f8f6f4 v[42:45], v[10:17], v[218:225], 0
	s_setprio 0
	s_barrier
	s_add_u32 s48, s46, 0x40100
	s_addc_u32 s49, s47, 0
	s_add_i32 s72, s65, s41
	v_lshl_add_u64 v[2:3], s[48:49], 0, v[164:165]
	s_mov_b32 m0, s72
	s_add_i32 s73, s72, 0x2000
	global_load_lds_dwordx4 v[2:3], off
	v_lshl_add_u64 v[2:3], s[48:49], 0, v[168:169]
	s_mov_b32 m0, s73
	s_nop 0
	global_load_lds_dwordx4 v[2:3], off
	s_waitcnt vmcnt(6)
	s_barrier
	s_setprio 1
	v_mfma_f32_16x16x128_f8f6f4 v[106:109], v[186:193], v[34:41], 0
	v_mfma_f32_16x16x128_f8f6f4 v[98:101], v[194:201], v[34:41], 0
	v_mfma_f32_16x16x128_f8f6f4 v[74:77], v[186:193], v[202:209], 0
	v_mfma_f32_16x16x128_f8f6f4 v[66:69], v[194:201], v[202:209], 0
	v_mfma_f32_16x16x128_f8f6f4 v[58:61], v[186:193], v[210:217], 0
	v_mfma_f32_16x16x128_f8f6f4 v[50:53], v[194:201], v[210:217], 0
	v_mfma_f32_16x16x128_f8f6f4 v[38:41], v[186:193], v[218:225], 0
	v_mfma_f32_16x16x128_f8f6f4 v[34:37], v[194:201], v[218:225], 0
	s_setprio 0
	s_add_i32 s74, 0, 0x18000
	v_add_u32_e32 v186, s74, v182
	s_barrier
	ds_read_b128 v[2:5], v186
	ds_read_b128 v[6:9], v186 offset:1024
	ds_read_b128 v[10:13], v186 offset:2048
	ds_read_b128 v[14:17], v186 offset:3072
	s_add_u32 s48, s44, 0x40100
	s_addc_u32 s49, s45, 0
	s_mov_b32 m0, s56
	v_lshl_add_u64 v[220:221], s[48:49], 0, v[162:163]
	ds_read_b128 v[188:191], v184 offset:32768
	ds_read_b128 v[192:195], v184 offset:33792
	ds_read_b128 v[196:199], v184 offset:34816
	ds_read_b128 v[200:203], v184 offset:35840
	ds_read_b128 v[204:207], v184 offset:36864
	ds_read_b128 v[208:211], v184 offset:37888
	ds_read_b128 v[212:215], v184 offset:38912
	ds_read_b128 v[216:219], v184 offset:39936
	global_load_lds_dwordx4 v[220:221], off
	v_lshl_add_u64 v[220:221], s[48:49], 0, v[166:167]
	s_mov_b32 m0, s57
	s_nop 0
	global_load_lds_dwordx4 v[220:221], off
	s_waitcnt lgkmcnt(8)
	s_barrier
	s_waitcnt lgkmcnt(0)
	s_setprio 1
	s_waitcnt lgkmcnt(0)
	v_mfma_f32_16x16x128_f8f6f4 v[150:153], v[2:9], v[188:195], v[150:153]
	v_mfma_f32_16x16x128_f8f6f4 v[146:149], v[10:17], v[188:195], v[146:149]
	v_mfma_f32_16x16x128_f8f6f4 v[134:137], v[2:9], v[196:203], v[134:137]
	v_mfma_f32_16x16x128_f8f6f4 v[130:133], v[10:17], v[196:203], v[130:133]
	v_mfma_f32_16x16x128_f8f6f4 v[118:121], v[2:9], v[204:211], v[118:121]
	v_mfma_f32_16x16x128_f8f6f4 v[114:117], v[10:17], v[204:211], v[114:117]
	v_mfma_f32_16x16x128_f8f6f4 v[86:89], v[2:9], v[212:219], v[86:89]
	v_mfma_f32_16x16x128_f8f6f4 v[82:85], v[10:17], v[212:219], v[82:85]
	s_setprio 0
	s_barrier
	s_add_i32 s76, 0, 0x1c000
	s_add_i32 s74, s74, s41
	v_add_u32_e32 v187, s76, v182
	v_lshl_add_u64 v[178:179], v[178:179], 0, s[16:17]
	s_mov_b32 m0, s74
	s_add_i32 s75, s74, 0x2000
	ds_read_b128 v[220:223], v187
	ds_read_b128 v[224:227], v187 offset:1024
	ds_read_b128 v[228:231], v187 offset:2048
	ds_read_b128 v[232:235], v187 offset:3072
	global_load_lds_dwordx4 v[178:179], off
	v_lshl_add_u64 v[178:179], v[180:181], 0, s[16:17]
	s_mov_b32 m0, s75
	s_nop 0
	global_load_lds_dwordx4 v[178:179], off
	s_barrier
	s_waitcnt lgkmcnt(0)
	s_setprio 1
	s_waitcnt lgkmcnt(0)
	v_mfma_f32_16x16x128_f8f6f4 v[158:161], v[220:227], v[188:195], v[158:161]
	v_mfma_f32_16x16x128_f8f6f4 v[154:157], v[228:235], v[188:195], v[154:157]
	v_mfma_f32_16x16x128_f8f6f4 v[142:145], v[220:227], v[196:203], v[142:145]
	v_mfma_f32_16x16x128_f8f6f4 v[138:141], v[228:235], v[196:203], v[138:141]
	v_mfma_f32_16x16x128_f8f6f4 v[126:129], v[220:227], v[204:211], v[126:129]
	v_mfma_f32_16x16x128_f8f6f4 v[122:125], v[228:235], v[204:211], v[122:125]
	v_mfma_f32_16x16x128_f8f6f4 v[94:97], v[220:227], v[212:219], v[94:97]
	v_mfma_f32_16x16x128_f8f6f4 v[90:93], v[228:235], v[212:219], v[90:93]
	s_setprio 0
	s_mov_b32 m0, s59
	v_lshl_add_u64 v[174:175], v[174:175], 0, s[16:17]
	s_barrier
	ds_read_b128 v[188:191], v184 offset:49152
	ds_read_b128 v[192:195], v184 offset:50176
	ds_read_b128 v[196:199], v184 offset:51200
	ds_read_b128 v[200:203], v184 offset:52224
	ds_read_b128 v[204:207], v184 offset:53248
	ds_read_b128 v[208:211], v184 offset:54272
	ds_read_b128 v[212:215], v184 offset:55296
	ds_read_b128 v[216:219], v184 offset:56320
	global_load_lds_dwordx4 v[174:175], off
	v_lshl_add_u64 v[174:175], v[176:177], 0, s[16:17]
	s_mov_b32 m0, s60
	s_nop 0
	global_load_lds_dwordx4 v[174:175], off
	s_barrier
	s_waitcnt lgkmcnt(0)
	s_setprio 1
	s_waitcnt lgkmcnt(0)
	v_mfma_f32_16x16x128_f8f6f4 v[110:113], v[2:9], v[188:195], v[110:113]
	v_mfma_f32_16x16x128_f8f6f4 v[102:105], v[10:17], v[188:195], v[102:105]
	v_mfma_f32_16x16x128_f8f6f4 v[78:81], v[2:9], v[196:203], v[78:81]
	v_mfma_f32_16x16x128_f8f6f4 v[70:73], v[10:17], v[196:203], v[70:73]
	v_mfma_f32_16x16x128_f8f6f4 v[62:65], v[2:9], v[204:211], v[62:65]
	v_mfma_f32_16x16x128_f8f6f4 v[54:57], v[10:17], v[204:211], v[54:57]
	v_mfma_f32_16x16x128_f8f6f4 v[46:49], v[2:9], v[212:219], v[46:49]
	v_mfma_f32_16x16x128_f8f6f4 v[42:45], v[10:17], v[212:219], v[42:45]
	s_setprio 0
	s_barrier
	s_add_u32 s48, s46, 0x40180
	s_addc_u32 s49, s47, 0
	s_add_i32 s76, s76, s41
	v_lshl_add_u64 v[2:3], s[48:49], 0, v[164:165]
	s_mov_b32 m0, s76
	s_add_i32 s77, s76, 0x2000
	global_load_lds_dwordx4 v[2:3], off
	v_lshl_add_u64 v[2:3], s[48:49], 0, v[168:169]
	s_mov_b32 m0, s77
	s_nop 0
	global_load_lds_dwordx4 v[2:3], off
	s_waitcnt vmcnt(6)
	s_barrier
	s_setprio 1
	v_mfma_f32_16x16x128_f8f6f4 v[106:109], v[220:227], v[188:195], v[106:109]
	v_mfma_f32_16x16x128_f8f6f4 v[98:101], v[228:235], v[188:195], v[98:101]
	v_mfma_f32_16x16x128_f8f6f4 v[74:77], v[220:227], v[196:203], v[74:77]
	v_mfma_f32_16x16x128_f8f6f4 v[66:69], v[228:235], v[196:203], v[66:69]
	v_mfma_f32_16x16x128_f8f6f4 v[58:61], v[220:227], v[204:211], v[58:61]
	v_mfma_f32_16x16x128_f8f6f4 v[50:53], v[228:235], v[204:211], v[50:53]
	v_mfma_f32_16x16x128_f8f6f4 v[38:41], v[220:227], v[212:219], v[38:41]
	v_mfma_f32_16x16x128_f8f6f4 v[34:37], v[228:235], v[212:219], v[34:37]
	s_setprio 0
	s_add_u32 s44, s44, 0x40180
	s_addc_u32 s45, s45, 0
	s_add_u32 s78, s46, 0x200
	s_addc_u32 s79, s47, 0
	s_mov_b32 s80, 0
	s_barrier
.LBB0_1547:
	ds_read_b128 v[10:13], v183
	ds_read_b128 v[14:17], v183 offset:1024
	ds_read_b128 v[174:177], v183 offset:2048
	ds_read_b128 v[178:181], v183 offset:3072
	s_add_u32 s46, s44, 0xfffc0080
	s_addc_u32 s47, s45, -1
	s_cmp_eq_u32 s80, 12
	s_cselect_b32 s49, s27, s47
	s_cselect_b32 s48, s31, s46
	s_cselect_b32 s47, s25, s79
	s_cselect_b32 s46, s39, s78
	s_mov_b32 m0, s68
	v_lshl_add_u64 v[2:3], s[44:45], 0, v[170:171]
	ds_read_b128 v[188:191], v184
	ds_read_b128 v[192:195], v184 offset:1024
	ds_read_b128 v[196:199], v184 offset:2048
	ds_read_b128 v[200:203], v184 offset:3072
	ds_read_b128 v[204:207], v184 offset:4096
	ds_read_b128 v[208:211], v184 offset:5120
	ds_read_b128 v[212:215], v184 offset:6144
	ds_read_b128 v[216:219], v184 offset:7168
	global_load_lds_dwordx4 v[2:3], off
	v_lshl_add_u64 v[2:3], s[44:45], 0, v[172:173]
	s_mov_b32 m0, s69
	s_nop 0
	global_load_lds_dwordx4 v[2:3], off
	ds_read_b128 v[220:223], v185
	ds_read_b128 v[224:227], v185 offset:1024
	ds_read_b128 v[228:231], v185 offset:2048
	ds_read_b128 v[232:235], v185 offset:3072
	s_waitcnt vmcnt(8) lgkmcnt(0)
	s_barrier
	s_setprio 1
	v_mfma_f32_16x16x128_f8f6f4 v[150:153], v[10:17], v[188:195], v[150:153]
	v_mfma_f32_16x16x128_f8f6f4 v[146:149], v[174:181], v[188:195], v[146:149]
	v_mfma_f32_16x16x128_f8f6f4 v[134:137], v[10:17], v[196:203], v[134:137]
	v_mfma_f32_16x16x128_f8f6f4 v[130:133], v[174:181], v[196:203], v[130:133]
	v_mfma_f32_16x16x128_f8f6f4 v[118:121], v[10:17], v[204:211], v[118:121]
	v_mfma_f32_16x16x128_f8f6f4 v[114:117], v[174:181], v[204:211], v[114:117]
	v_mfma_f32_16x16x128_f8f6f4 v[86:89], v[10:17], v[212:219], v[86:89]
	v_mfma_f32_16x16x128_f8f6f4 v[82:85], v[174:181], v[212:219], v[82:85]
	v_mfma_f32_16x16x128_f8f6f4 v[158:161], v[220:227], v[188:195], v[158:161]
	v_mfma_f32_16x16x128_f8f6f4 v[154:157], v[228:235], v[188:195], v[154:157]
	v_mfma_f32_16x16x128_f8f6f4 v[142:145], v[220:227], v[196:203], v[142:145]
	v_mfma_f32_16x16x128_f8f6f4 v[138:141], v[228:235], v[196:203], v[138:141]
	v_mfma_f32_16x16x128_f8f6f4 v[126:129], v[220:227], v[204:211], v[126:129]
	v_mfma_f32_16x16x128_f8f6f4 v[122:125], v[228:235], v[204:211], v[122:125]
	v_mfma_f32_16x16x128_f8f6f4 v[94:97], v[220:227], v[212:219], v[94:97]
	v_mfma_f32_16x16x128_f8f6f4 v[90:93], v[228:235], v[212:219], v[90:93]
	s_setprio 0
	s_barrier
	ds_read_b128 v[188:191], v184 offset:16384
	ds_read_b128 v[192:195], v184 offset:17408
	ds_read_b128 v[196:199], v184 offset:18432
	ds_read_b128 v[200:203], v184 offset:19456
	ds_read_b128 v[204:207], v184 offset:20480
	ds_read_b128 v[208:211], v184 offset:21504
	ds_read_b128 v[212:215], v184 offset:22528
	ds_read_b128 v[216:219], v184 offset:23552
	s_mov_b32 m0, s70
	v_lshl_add_u64 v[6:7], s[46:47], 0, v[164:165]
	global_load_lds_dwordx4 v[6:7], off
	v_lshl_add_u64 v[8:9], s[46:47], 0, v[168:169]
	s_mov_b32 m0, s71
	s_nop 0
	global_load_lds_dwordx4 v[8:9], off
	s_mov_b32 m0, s54
	v_lshl_add_u64 v[2:3], s[48:49], 0, v[162:163]
	global_load_lds_dwordx4 v[2:3], off
	v_lshl_add_u64 v[4:5], s[48:49], 0, v[166:167]
	s_mov_b32 m0, s55
	s_nop 0
	global_load_lds_dwordx4 v[4:5], off
	s_add_u32 s82, s46, 0x40000
	s_addc_u32 s83, s47, 0
	s_mov_b32 m0, s72
	v_lshl_add_u64 v[236:237], s[82:83], 0, v[164:165]
	global_load_lds_dwordx4 v[236:237], off
	v_lshl_add_u64 v[236:237], s[82:83], 0, v[168:169]
	s_mov_b32 m0, s73
	s_nop 0
	global_load_lds_dwordx4 v[236:237], off
	s_waitcnt vmcnt(8) lgkmcnt(0)
	s_barrier
	s_setprio 1
	v_mfma_f32_16x16x128_f8f6f4 v[110:113], v[10:17], v[188:195], v[110:113]
	v_mfma_f32_16x16x128_f8f6f4 v[102:105], v[174:181], v[188:195], v[102:105]
	v_mfma_f32_16x16x128_f8f6f4 v[78:81], v[10:17], v[196:203], v[78:81]
	v_mfma_f32_16x16x128_f8f6f4 v[70:73], v[174:181], v[196:203], v[70:73]
	v_mfma_f32_16x16x128_f8f6f4 v[62:65], v[10:17], v[204:211], v[62:65]
	v_mfma_f32_16x16x128_f8f6f4 v[54:57], v[174:181], v[204:211], v[54:57]
	v_mfma_f32_16x16x128_f8f6f4 v[46:49], v[10:17], v[212:219], v[46:49]
	v_mfma_f32_16x16x128_f8f6f4 v[42:45], v[174:181], v[212:219], v[42:45]
	v_mfma_f32_16x16x128_f8f6f4 v[106:109], v[220:227], v[188:195], v[106:109]
	v_mfma_f32_16x16x128_f8f6f4 v[98:101], v[228:235], v[188:195], v[98:101]
	v_mfma_f32_16x16x128_f8f6f4 v[74:77], v[220:227], v[196:203], v[74:77]
	v_mfma_f32_16x16x128_f8f6f4 v[66:69], v[228:235], v[196:203], v[66:69]
	v_mfma_f32_16x16x128_f8f6f4 v[58:61], v[220:227], v[204:211], v[58:61]
	v_mfma_f32_16x16x128_f8f6f4 v[50:53], v[228:235], v[204:211], v[50:53]
	v_mfma_f32_16x16x128_f8f6f4 v[38:41], v[220:227], v[212:219], v[38:41]
	v_mfma_f32_16x16x128_f8f6f4 v[34:37], v[228:235], v[212:219], v[34:37]
	s_setprio 0
	s_barrier
	ds_read_b128 v[10:13], v186
	ds_read_b128 v[14:17], v186 offset:1024
	ds_read_b128 v[174:177], v186 offset:2048
	ds_read_b128 v[178:181], v186 offset:3072
	s_add_u32 s48, s48, 0x40000
	s_addc_u32 s49, s49, 0
	s_mov_b32 m0, s56
	v_lshl_add_u64 v[220:221], s[48:49], 0, v[162:163]
	ds_read_b128 v[188:191], v184 offset:32768
	ds_read_b128 v[192:195], v184 offset:33792
	ds_read_b128 v[196:199], v184 offset:34816
	ds_read_b128 v[200:203], v184 offset:35840
	ds_read_b128 v[204:207], v184 offset:36864
	ds_read_b128 v[208:211], v184 offset:37888
	ds_read_b128 v[212:215], v184 offset:38912
	ds_read_b128 v[216:219], v184 offset:39936
	global_load_lds_dwordx4 v[220:221], off
	v_lshl_add_u64 v[220:221], s[48:49], 0, v[166:167]
	s_mov_b32 m0, s57
	s_nop 0
	global_load_lds_dwordx4 v[220:221], off
	ds_read_b128 v[220:223], v187
	ds_read_b128 v[224:227], v187 offset:1024
	ds_read_b128 v[228:231], v187 offset:2048
	ds_read_b128 v[232:235], v187 offset:3072
	s_waitcnt vmcnt(8) lgkmcnt(0)
	s_barrier
	s_setprio 1
	v_mfma_f32_16x16x128_f8f6f4 v[150:153], v[10:17], v[188:195], v[150:153]
	v_mfma_f32_16x16x128_f8f6f4 v[146:149], v[174:181], v[188:195], v[146:149]
	v_mfma_f32_16x16x128_f8f6f4 v[134:137], v[10:17], v[196:203], v[134:137]
	v_mfma_f32_16x16x128_f8f6f4 v[130:133], v[174:181], v[196:203], v[130:133]
	v_mfma_f32_16x16x128_f8f6f4 v[118:121], v[10:17], v[204:211], v[118:121]
	v_mfma_f32_16x16x128_f8f6f4 v[114:117], v[174:181], v[204:211], v[114:117]
	v_mfma_f32_16x16x128_f8f6f4 v[86:89], v[10:17], v[212:219], v[86:89]
	v_mfma_f32_16x16x128_f8f6f4 v[82:85], v[174:181], v[212:219], v[82:85]
	v_mfma_f32_16x16x128_f8f6f4 v[158:161], v[220:227], v[188:195], v[158:161]
	v_mfma_f32_16x16x128_f8f6f4 v[154:157], v[228:235], v[188:195], v[154:157]
	v_mfma_f32_16x16x128_f8f6f4 v[142:145], v[220:227], v[196:203], v[142:145]
	v_mfma_f32_16x16x128_f8f6f4 v[138:141], v[228:235], v[196:203], v[138:141]
	v_mfma_f32_16x16x128_f8f6f4 v[126:129], v[220:227], v[204:211], v[126:129]
	v_mfma_f32_16x16x128_f8f6f4 v[122:125], v[228:235], v[204:211], v[122:125]
	v_mfma_f32_16x16x128_f8f6f4 v[94:97], v[220:227], v[212:219], v[94:97]
	v_mfma_f32_16x16x128_f8f6f4 v[90:93], v[228:235], v[212:219], v[90:93]
	s_setprio 0
	s_barrier
	ds_read_b128 v[188:191], v184 offset:49152
	ds_read_b128 v[192:195], v184 offset:50176
	ds_read_b128 v[196:199], v184 offset:51200
	ds_read_b128 v[200:203], v184 offset:52224
	ds_read_b128 v[204:207], v184 offset:53248
	ds_read_b128 v[208:211], v184 offset:54272
	ds_read_b128 v[212:215], v184 offset:55296
	ds_read_b128 v[216:219], v184 offset:56320
	s_mov_b32 m0, s74
	v_lshl_add_u64 v[6:7], v[6:7], 0, s[10:11]
	global_load_lds_dwordx4 v[6:7], off
	v_lshl_add_u64 v[6:7], v[8:9], 0, s[10:11]
	s_mov_b32 m0, s75
	s_nop 0
	global_load_lds_dwordx4 v[6:7], off
	s_mov_b32 m0, s59
	v_lshl_add_u64 v[2:3], v[2:3], 0, s[10:11]
	global_load_lds_dwordx4 v[2:3], off
	v_lshl_add_u64 v[2:3], v[4:5], 0, s[10:11]
	s_mov_b32 m0, s60
	s_nop 0
	global_load_lds_dwordx4 v[2:3], off
	s_add_u32 s46, s46, 0x40080
	s_addc_u32 s47, s47, 0
	s_mov_b32 m0, s76
	v_lshl_add_u64 v[2:3], s[46:47], 0, v[164:165]
	global_load_lds_dwordx4 v[2:3], off
	v_lshl_add_u64 v[2:3], s[46:47], 0, v[168:169]
	s_mov_b32 m0, s77
	s_nop 0
	global_load_lds_dwordx4 v[2:3], off
	s_waitcnt vmcnt(8) lgkmcnt(0)
	s_barrier
	s_setprio 1
	v_mfma_f32_16x16x128_f8f6f4 v[110:113], v[10:17], v[188:195], v[110:113]
	v_mfma_f32_16x16x128_f8f6f4 v[102:105], v[174:181], v[188:195], v[102:105]
	v_mfma_f32_16x16x128_f8f6f4 v[78:81], v[10:17], v[196:203], v[78:81]
	v_mfma_f32_16x16x128_f8f6f4 v[70:73], v[174:181], v[196:203], v[70:73]
	v_mfma_f32_16x16x128_f8f6f4 v[62:65], v[10:17], v[204:211], v[62:65]
	v_mfma_f32_16x16x128_f8f6f4 v[54:57], v[174:181], v[204:211], v[54:57]
	v_mfma_f32_16x16x128_f8f6f4 v[46:49], v[10:17], v[212:219], v[46:49]
	v_mfma_f32_16x16x128_f8f6f4 v[42:45], v[174:181], v[212:219], v[42:45]
	v_mfma_f32_16x16x128_f8f6f4 v[106:109], v[220:227], v[188:195], v[106:109]
	v_mfma_f32_16x16x128_f8f6f4 v[98:101], v[228:235], v[188:195], v[98:101]
	v_mfma_f32_16x16x128_f8f6f4 v[74:77], v[220:227], v[196:203], v[74:77]
	v_mfma_f32_16x16x128_f8f6f4 v[66:69], v[228:235], v[196:203], v[66:69]
	v_mfma_f32_16x16x128_f8f6f4 v[58:61], v[220:227], v[204:211], v[58:61]
	v_mfma_f32_16x16x128_f8f6f4 v[50:53], v[228:235], v[204:211], v[50:53]
	v_mfma_f32_16x16x128_f8f6f4 v[38:41], v[220:227], v[212:219], v[38:41]
	v_mfma_f32_16x16x128_f8f6f4 v[34:37], v[228:235], v[212:219], v[34:37]
	s_setprio 0
	s_add_i32 s80, s80, 2
	s_add_u32 s44, s44, 0x100
	s_addc_u32 s45, s45, 0
	s_add_u32 s78, s78, 0x100
	s_addc_u32 s79, s79, 0
	s_cmp_gt_u32 s80, 13
	s_barrier
	s_cbranch_scc0 .LBB0_1547
	v_mov_b32_e32 v2, v0
	s_nop 15
	s_nop 15
	s_lshl_b32 s27, s40, 8
	v_readfirstlane_b32 s25, v2
	s_ashr_i32 s31, s25, 2
	s_andn2_b32 s31, s31, 63
	s_add_i32 s31, s31, s27
	s_lshr_b32 s25, s25, 1
	v_and_or_b32 v10, v2, 15, s31
	s_and_b32 s25, s25, 0x60
	v_lshrrev_b32_e32 v2, 1, v2
	s_lshl_b32 s27, s38, 8
	v_and_b32_e32 v4, 24, v2
	s_or_b32 s27, s25, s27
	v_or_b32_e32 v2, s27, v4
	v_ashrrev_i32_e32 v11, 31, v10
	v_ashrrev_i32_e32 v3, 31, v2
	v_lshlrev_b64 v[6:7], 12, v[10:11]
	v_lshl_add_u64 v[6:7], s[8:9], 0, v[6:7]
	v_lshlrev_b64 v[12:13], 1, v[2:3]
	s_waitcnt vmcnt(6)
	v_lshl_add_u64 v[2:3], v[6:7], 0, v[12:13]
	v_pk_fma_f32 v[6:7], v[150:151], s[18:19], v[22:23] op_sel_hi:[1,0,1]
	v_pk_fma_f32 v[8:9], v[152:153], s[18:19], v[24:25] op_sel_hi:[1,0,1]
	v_cvt_pk_bf16_f32 v6, v6, v7
	v_pk_fma_f32 v[14:15], v[148:149], s[18:19], v[20:21] op_sel_hi:[1,0,1]
	v_cvt_pk_bf16_f32 v7, v8, v9
	v_pk_fma_f32 v[16:17], v[146:147], s[18:19], v[18:19] op_sel_hi:[1,0,1]
	v_pk_fma_f32 v[130:131], v[130:131], s[18:19], v[18:19] op_sel_hi:[1,0,1]
	v_cvt_pk_bf16_f32 v8, v16, v17
	v_cvt_pk_bf16_f32 v9, v14, v15
	global_store_dwordx4 v[2:3], v[6:9], off
	v_pk_fma_f32 v[14:15], v[156:157], s[18:19], v[28:29] op_sel_hi:[1,0,1]
	v_pk_fma_f32 v[16:17], v[154:155], s[18:19], v[26:27] op_sel_hi:[1,0,1]
	v_pk_fma_f32 v[6:7], v[158:159], s[18:19], v[30:31] op_sel_hi:[1,0,1]
	v_pk_fma_f32 v[8:9], v[160:161], s[18:19], v[32:33] op_sel_hi:[1,0,1]
	v_cvt_pk_bf16_f32 v6, v6, v7
	v_pk_fma_f32 v[114:115], v[114:115], s[18:19], v[18:19] op_sel_hi:[1,0,1]
	v_cvt_pk_bf16_f32 v7, v8, v9
	v_cvt_pk_bf16_f32 v8, v16, v17
	v_cvt_pk_bf16_f32 v9, v14, v15
	global_store_dwordx4 v[2:3], v[6:9], off offset:256
	v_pk_fma_f32 v[16:17], v[132:133], s[18:19], v[20:21] op_sel_hi:[1,0,1]
	s_mov_b32 s27, 0x80000
	v_or_b32_e32 v6, 16, v10
	v_ashrrev_i32_e32 v7, 31, v6
	v_lshlrev_b64 v[6:7], 12, v[6:7]
	v_lshl_add_u64 v[6:7], s[8:9], 0, v[6:7]
	v_lshl_add_u64 v[14:15], v[6:7], 0, v[12:13]
	v_pk_fma_f32 v[6:7], v[134:135], s[18:19], v[22:23] op_sel_hi:[1,0,1]
	v_pk_fma_f32 v[8:9], v[136:137], s[18:19], v[24:25] op_sel_hi:[1,0,1]
	v_cvt_pk_bf16_f32 v6, v6, v7
	s_mov_b64 s[38:39], 0x80000
	v_cvt_pk_bf16_f32 v7, v8, v9
	v_cvt_pk_bf16_f32 v8, v130, v131
	v_cvt_pk_bf16_f32 v9, v16, v17
	global_store_dwordx4 v[14:15], v[6:9], off
	v_pk_fma_f32 v[16:17], v[140:141], s[18:19], v[28:29] op_sel_hi:[1,0,1]
	v_pk_fma_f32 v[130:131], v[138:139], s[18:19], v[26:27] op_sel_hi:[1,0,1]
	v_pk_fma_f32 v[6:7], v[142:143], s[18:19], v[30:31] op_sel_hi:[1,0,1]
	v_pk_fma_f32 v[8:9], v[144:145], s[18:19], v[32:33] op_sel_hi:[1,0,1]
	v_cvt_pk_bf16_f32 v6, v6, v7
	v_readlane_b32 s68, v254, 0
	v_cvt_pk_bf16_f32 v7, v8, v9
	v_cvt_pk_bf16_f32 v8, v130, v131
	v_cvt_pk_bf16_f32 v9, v16, v17
	global_store_dwordx4 v[14:15], v[6:9], off offset:256
	v_pk_fma_f32 v[16:17], v[116:117], s[18:19], v[20:21] op_sel_hi:[1,0,1]
	v_readlane_b32 s69, v254, 1
	v_or_b32_e32 v6, 32, v10
	v_ashrrev_i32_e32 v7, 31, v6
	v_lshlrev_b64 v[6:7], 12, v[6:7]
	v_lshl_add_u64 v[6:7], s[8:9], 0, v[6:7]
	v_lshl_add_u64 v[14:15], v[6:7], 0, v[12:13]
	v_pk_fma_f32 v[6:7], v[118:119], s[18:19], v[22:23] op_sel_hi:[1,0,1]
	v_pk_fma_f32 v[8:9], v[120:121], s[18:19], v[24:25] op_sel_hi:[1,0,1]
	v_cvt_pk_bf16_f32 v6, v6, v7
	v_readlane_b32 s70, v254, 2
	v_cvt_pk_bf16_f32 v7, v8, v9
	v_cvt_pk_bf16_f32 v8, v114, v115
	v_cvt_pk_bf16_f32 v9, v16, v17
	global_store_dwordx4 v[14:15], v[6:9], off
	v_pk_fma_f32 v[16:17], v[124:125], s[18:19], v[28:29] op_sel_hi:[1,0,1]
	v_pk_fma_f32 v[114:115], v[122:123], s[18:19], v[26:27] op_sel_hi:[1,0,1]
	v_pk_fma_f32 v[6:7], v[126:127], s[18:19], v[30:31] op_sel_hi:[1,0,1]
	v_pk_fma_f32 v[8:9], v[128:129], s[18:19], v[32:33] op_sel_hi:[1,0,1]
	v_cvt_pk_bf16_f32 v6, v6, v7
	v_readlane_b32 s71, v254, 3
	v_cvt_pk_bf16_f32 v7, v8, v9
	v_cvt_pk_bf16_f32 v8, v114, v115
	v_cvt_pk_bf16_f32 v9, v16, v17
	global_store_dwordx4 v[14:15], v[6:9], off offset:256
	v_pk_fma_f32 v[14:15], v[82:83], s[18:19], v[18:19] op_sel_hi:[1,0,1]
	v_readlane_b32 s72, v254, 4
	v_or_b32_e32 v6, 48, v10
	v_ashrrev_i32_e32 v7, 31, v6
	v_lshlrev_b64 v[6:7], 12, v[6:7]
	v_lshl_add_u64 v[6:7], s[8:9], 0, v[6:7]
	v_lshl_add_u64 v[10:11], v[6:7], 0, v[12:13]
	v_pk_fma_f32 v[8:9], v[88:89], s[18:19], v[24:25] op_sel_hi:[1,0,1]
	v_pk_fma_f32 v[6:7], v[86:87], s[18:19], v[22:23] op_sel_hi:[1,0,1]
	v_pk_fma_f32 v[12:13], v[84:85], s[18:19], v[20:21] op_sel_hi:[1,0,1]
	v_cvt_pk_bf16_f32 v6, v6, v7
	v_cvt_pk_bf16_f32 v7, v8, v9
	v_cvt_pk_bf16_f32 v8, v14, v15
	v_pk_fma_f32 v[14:15], v[90:91], s[18:19], v[26:27] op_sel_hi:[1,0,1]
	v_cvt_pk_bf16_f32 v9, v12, v13
	global_store_dwordx4 v[10:11], v[6:9], off
	v_pk_fma_f32 v[12:13], v[92:93], s[18:19], v[28:29] op_sel_hi:[1,0,1]
	v_readlane_b32 s73, v254, 5
	v_pk_fma_f32 v[8:9], v[96:97], s[18:19], v[32:33] op_sel_hi:[1,0,1]
	v_pk_fma_f32 v[6:7], v[94:95], s[18:19], v[30:31] op_sel_hi:[1,0,1]
	v_readlane_b32 s74, v254, 6
	v_cvt_pk_bf16_f32 v6, v6, v7
	v_cvt_pk_bf16_f32 v7, v8, v9
	v_cvt_pk_bf16_f32 v8, v14, v15
	v_cvt_pk_bf16_f32 v9, v12, v13
	global_store_dwordx4 v[10:11], v[6:9], off offset:256
	v_pk_fma_f32 v[12:13], v[104:105], s[18:19], v[20:21] op_sel_hi:[1,0,1]
	v_pk_fma_f32 v[14:15], v[102:103], s[18:19], v[18:19] op_sel_hi:[1,0,1]
	v_pk_fma_f32 v[8:9], v[112:113], s[18:19], v[24:25] op_sel_hi:[1,0,1]
	v_pk_fma_f32 v[6:7], v[110:111], s[18:19], v[22:23] op_sel_hi:[1,0,1]
	v_lshl_add_u64 v[10:11], v[2:3], 0, s[38:39]
	v_cvt_pk_bf16_f32 v6, v6, v7
	v_cvt_pk_bf16_f32 v7, v8, v9
	v_cvt_pk_bf16_f32 v8, v14, v15
	v_cvt_pk_bf16_f32 v9, v12, v13
	v_add_co_u32_e32 v12, vcc, s27, v2
	v_pk_fma_f32 v[14:15], v[98:99], s[18:19], v[26:27] op_sel_hi:[1,0,1]
	s_nop 0
	v_addc_co_u32_e32 v13, vcc, 0, v3, vcc
	global_store_dwordx4 v[12:13], v[6:9], off
	v_pk_fma_f32 v[12:13], v[100:101], s[18:19], v[28:29] op_sel_hi:[1,0,1]
	s_mov_b32 s27, 0x90000
	v_pk_fma_f32 v[8:9], v[108:109], s[18:19], v[32:33] op_sel_hi:[1,0,1]
	v_pk_fma_f32 v[6:7], v[106:107], s[18:19], v[30:31] op_sel_hi:[1,0,1]
	s_mov_b64 s[38:39], 0x90000
	v_cvt_pk_bf16_f32 v6, v6, v7
	v_cvt_pk_bf16_f32 v7, v8, v9
	v_cvt_pk_bf16_f32 v8, v14, v15
	v_cvt_pk_bf16_f32 v9, v12, v13
	global_store_dwordx4 v[10:11], v[6:9], off offset:256
	v_pk_fma_f32 v[12:13], v[72:73], s[18:19], v[20:21] op_sel_hi:[1,0,1]
	v_pk_fma_f32 v[14:15], v[70:71], s[18:19], v[18:19] op_sel_hi:[1,0,1]
	v_pk_fma_f32 v[8:9], v[80:81], s[18:19], v[24:25] op_sel_hi:[1,0,1]
	v_pk_fma_f32 v[6:7], v[78:79], s[18:19], v[22:23] op_sel_hi:[1,0,1]
	v_lshl_add_u64 v[10:11], v[2:3], 0, s[38:39]
	v_cvt_pk_bf16_f32 v6, v6, v7
	v_cvt_pk_bf16_f32 v7, v8, v9
	v_cvt_pk_bf16_f32 v8, v14, v15
	v_cvt_pk_bf16_f32 v9, v12, v13
	v_add_co_u32_e32 v12, vcc, s27, v2
	v_pk_fma_f32 v[14:15], v[66:67], s[18:19], v[26:27] op_sel_hi:[1,0,1]
	s_nop 0
	v_addc_co_u32_e32 v13, vcc, 0, v3, vcc
	global_store_dwordx4 v[12:13], v[6:9], off
	v_pk_fma_f32 v[12:13], v[68:69], s[18:19], v[28:29] op_sel_hi:[1,0,1]
	s_mov_b64 s[38:39], 0xa0000
	v_pk_fma_f32 v[8:9], v[76:77], s[18:19], v[32:33] op_sel_hi:[1,0,1]
	v_pk_fma_f32 v[6:7], v[74:75], s[18:19], v[30:31] op_sel_hi:[1,0,1]
	v_readlane_b32 s75, v254, 7
	v_cvt_pk_bf16_f32 v6, v6, v7
	v_cvt_pk_bf16_f32 v7, v8, v9
	v_cvt_pk_bf16_f32 v8, v14, v15
	v_cvt_pk_bf16_f32 v9, v12, v13
	global_store_dwordx4 v[10:11], v[6:9], off offset:256
	v_pk_fma_f32 v[12:13], v[56:57], s[18:19], v[20:21] op_sel_hi:[1,0,1]
	v_pk_fma_f32 v[14:15], v[54:55], s[18:19], v[18:19] op_sel_hi:[1,0,1]
	v_pk_fma_f32 v[8:9], v[64:65], s[18:19], v[24:25] op_sel_hi:[1,0,1]
	v_pk_fma_f32 v[6:7], v[62:63], s[18:19], v[22:23] op_sel_hi:[1,0,1]
	v_lshl_add_u64 v[10:11], v[2:3], 0, s[38:39]
	v_cvt_pk_bf16_f32 v6, v6, v7
	v_cvt_pk_bf16_f32 v7, v8, v9
	v_cvt_pk_bf16_f32 v8, v14, v15
	v_cvt_pk_bf16_f32 v9, v12, v13
	v_add_co_u32_e32 v12, vcc, s66, v2
	v_pk_fma_f32 v[14:15], v[50:51], s[18:19], v[26:27] op_sel_hi:[1,0,1]
	s_nop 0
	v_addc_co_u32_e32 v13, vcc, 0, v3, vcc
	global_store_dwordx4 v[12:13], v[6:9], off
	v_pk_fma_f32 v[12:13], v[52:53], s[18:19], v[28:29] op_sel_hi:[1,0,1]
	s_mov_b64 s[38:39], -1
	v_pk_fma_f32 v[8:9], v[60:61], s[18:19], v[32:33] op_sel_hi:[1,0,1]
	v_pk_fma_f32 v[6:7], v[58:59], s[18:19], v[30:31] op_sel_hi:[1,0,1]
	s_nop 0
	v_cvt_pk_bf16_f32 v6, v6, v7
	v_cvt_pk_bf16_f32 v7, v8, v9
	v_cvt_pk_bf16_f32 v8, v14, v15
	v_cvt_pk_bf16_f32 v9, v12, v13
	global_store_dwordx4 v[10:11], v[6:9], off offset:256
	v_lshl_add_u64 v[10:11], v[2:3], 0, s[20:21]
	v_add_co_u32_e32 v2, vcc, s67, v2
	v_pk_fma_f32 v[8:9], v[48:49], s[18:19], v[24:25] op_sel_hi:[1,0,1]
	v_pk_fma_f32 v[6:7], v[46:47], s[18:19], v[22:23] op_sel_hi:[1,0,1]
	v_pk_fma_f32 v[12:13], v[44:45], s[18:19], v[20:21] op_sel_hi:[1,0,1]
	v_pk_fma_f32 v[14:15], v[42:43], s[18:19], v[18:19] op_sel_hi:[1,0,1]
	v_cvt_pk_bf16_f32 v6, v6, v7
	v_cvt_pk_bf16_f32 v7, v8, v9
	v_addc_co_u32_e32 v3, vcc, 0, v3, vcc
	v_cvt_pk_bf16_f32 v8, v14, v15
	v_cvt_pk_bf16_f32 v9, v12, v13
	global_store_dwordx4 v[2:3], v[6:9], off
	s_and_b64 vcc, s[42:43], exec
	v_pk_fma_f32 v[2:3], v[40:41], s[18:19], v[32:33] op_sel_hi:[1,0,1]
	v_pk_fma_f32 v[6:7], v[38:39], s[18:19], v[30:31] op_sel_hi:[1,0,1]
	v_pk_fma_f32 v[8:9], v[34:35], s[18:19], v[26:27] op_sel_hi:[1,0,1]
	v_pk_fma_f32 v[12:13], v[36:37], s[18:19], v[28:29] op_sel_hi:[1,0,1]
	v_cvt_pk_bf16_f32 v6, v6, v7
	v_cvt_pk_bf16_f32 v7, v2, v3
	v_cvt_pk_bf16_f32 v8, v8, v9
	s_nop 0
	v_cvt_pk_bf16_f32 v9, v12, v13
	global_store_dwordx4 v[10:11], v[6:9], off offset:256
	s_cbranch_vccz .LBB0_1541
	s_lshl_b32 s27, s24, 8
	s_or_b32 s25, s25, s27
	v_or_b32_e32 v2, s25, v4
	v_ashrrev_i32_e32 v3, 31, v2
	v_mov_b32_e32 v18, 0
	s_and_b64 vcc, exec, s[6:7]
	v_mov_b32_e32 v22, 0
	v_mov_b32_e32 v23, 0
	v_mov_b32_e32 v24, 0
	v_mov_b32_e32 v25, 0
	s_cbranch_vccnz .LBB0_1551
	s_ashr_i32 s27, s26, 31
	s_lshl_b64 s[38:39], s[26:27], 13
	s_add_u32 s38, s68, s38
	s_addc_u32 s39, s69, s39
	v_lshl_add_u64 v[4:5], v[2:3], 2, s[38:39]
	global_load_dwordx4 v[22:25], v[4:5], off
